# P3 GLA scan loads prefetched 8 chunks ahead (straight-line, counted vmcnt); SB attention K fragment loads all issued at top of iteration into 5 free quads; router top-4 rank count branch-free (cmp+cnd
# speedup vs baseline: 1.0057x; 1.0049x over previous
.LBB0_303:
	v_add_u32_e32 v66, s40, v167
	v_ashrrev_i32_e32 v67, 31, v66
	v_lshl_add_u64 v[68:69], s[40:41], 1, v[146:147]
	v_lshlrev_b64 v[66:67], 11, v[66:67]
	v_lshl_add_u64 v[174:175], v[68:69], 0, v[156:157]
	v_lshl_add_u64 v[116:117], v[150:151], 0, v[66:67]
	v_lshl_add_u64 v[70:71], v[68:69], 0, v[152:153]
	v_lshl_add_u64 v[72:73], v[68:69], 0, v[154:155]
	v_lshl_add_u64 v[178:179], v[68:69], 0, v[158:159]
	global_load_dwordx2 v[114:115], v[174:175], off
	global_load_dwordx2 v[126:127], v[70:71], off
	global_load_dwordx2 v[128:129], v[70:71], off offset:16
	global_load_dwordx2 v[118:119], v[70:71], off offset:32
	global_load_dwordx2 v[120:121], v[70:71], off offset:48
	global_load_dwordx2 v[130:131], v[72:73], off
	global_load_dwordx2 v[132:133], v[72:73], off offset:16
	global_load_dwordx2 v[122:123], v[72:73], off offset:32
	global_load_dwordx2 v[124:125], v[72:73], off offset:48
	global_load_dwordx4 v[66:69], v[116:117], off
	global_load_dwordx4 v[134:137], v[116:117], off offset:32
	global_load_dwordx4 v[138:141], v[116:117], off offset:64
	global_load_dwordx4 v[230:233], v[116:117], off offset:96
	global_load_dwordx4 v[238:241], v[116:117], off offset:128
	global_load_dwordx4 v[242:245], v[116:117], off offset:160
	global_load_dwordx4 v[246:249], v[116:117], off offset:192
	global_load_dwordx4 v[250:253], v[116:117], off offset:224
	v_add_u32_e32 v169, s40, v166
	v_or_b32_e32 v216, 3, v169
	v_or_b32_e32 v217, 16, v169
	v_or_b32_e32 v218, 24, v169
	v_or_b32_e32 v219, 17, v169
	v_or_b32_e32 v220, 25, v169
	v_or_b32_e32 v221, 18, v169
	v_or_b32_e32 v222, 26, v169
	v_or_b32_e32 v223, 19, v169
	v_or_b32_e32 v224, 27, v169
	v_add_u32_e32 v210, 8, v169
	v_or_b32_e32 v211, 9, v169
	v_or_b32_e32 v212, 1, v169
	v_or_b32_e32 v213, 10, v169
	v_or_b32_e32 v214, 2, v169
	v_or_b32_e32 v215, 11, v169
	v_cmp_lt_i32_e64 s[12:13], v216, v142
	v_cmp_lt_i32_e64 s[14:15], v218, v142
	v_cmp_lt_i32_e32 vcc, v217, v1
	v_cmp_lt_i32_e64 s[22:23], v220, v142
	v_cmp_lt_i32_e64 s[24:25], v219, v1
	v_cmp_lt_i32_e64 s[26:27], v222, v142
	v_cmp_lt_i32_e64 s[28:29], v221, v1
	v_cmp_lt_i32_e64 s[30:31], v224, v142
	v_cmp_lt_i32_e64 s[34:35], v223, v1
	v_cmp_lt_i32_e64 s[4:5], v169, v142
	v_cmp_lt_i32_e64 s[6:7], v210, v1
	v_cmp_lt_i32_e64 s[8:9], v212, v142
	v_cmp_lt_i32_e64 s[16:17], v211, v1
	v_cmp_lt_i32_e64 s[10:11], v214, v142
	v_cmp_lt_i32_e64 s[18:19], v213, v1
	v_cmp_lt_i32_e64 s[20:21], v215, v1
	v_add_f32_e32 v197, 0, v149
	s_waitcnt vmcnt(7)
	v_mfma_f32_32x32x16_bf16 v[66:81], v[66:69], v[82:85], 0
	s_waitcnt vmcnt(6)
	v_mfma_f32_32x32x16_bf16 v[66:81], v[134:137], v[86:89], v[66:81]
	s_waitcnt vmcnt(5)
	v_mfma_f32_32x32x16_bf16 v[66:81], v[138:141], v[90:93], v[66:81]
	s_waitcnt vmcnt(4)
	v_mfma_f32_32x32x16_bf16 v[66:81], v[230:233], v[94:97], v[66:81]
	s_waitcnt vmcnt(3)
	v_mfma_f32_32x32x16_bf16 v[66:81], v[238:241], v[98:101], v[66:81]
	s_waitcnt vmcnt(2)
	v_mfma_f32_32x32x16_bf16 v[66:81], v[242:245], v[102:105], v[66:81]
	s_waitcnt vmcnt(1)
	v_mfma_f32_32x32x16_bf16 v[66:81], v[246:249], v[106:109], v[66:81]
	s_waitcnt vmcnt(0)
	global_load_dwordx2 v[116:117], v[174:175], off offset:16
	global_load_dwordx2 v[138:139], v[174:175], off offset:32
	global_load_dwordx2 v[140:141], v[174:175], off offset:48
	s_nop 0
	global_load_dwordx2 v[174:175], v[178:179], off
	global_load_dwordx2 v[176:177], v[178:179], off offset:16
	global_load_dwordx2 v[134:135], v[178:179], off offset:32
	global_load_dwordx2 v[136:137], v[178:179], off offset:48
	v_mfma_f32_32x32x16_bf16 v[66:81], v[250:253], v[110:113], v[66:81]
	s_nop 11
	v_mul_f32_e32 v171, 0x3e0293ee, v66
	v_mul_f32_e32 v173, 0x3e0293ee, v67
	v_mul_f32_e32 v179, 0x3e0293ee, v68
	v_mul_f32_e32 v181, 0x3e0293ee, v69
	v_mul_f32_e32 v182, 0x3e0293ee, v70
	v_mul_f32_e32 v183, 0x3e0293ee, v71
	v_mul_f32_e32 v184, 0x3e0293ee, v72
	v_mul_f32_e32 v185, 0x3e0293ee, v73
	v_mul_f32_e32 v186, 0x3e0293ee, v74
	v_mul_f32_e32 v187, 0x3e0293ee, v75
	v_mul_f32_e32 v188, 0x3e0293ee, v76
	v_mul_f32_e32 v190, 0x3e0293ee, v77
	v_mul_f32_e32 v191, 0x3e0293ee, v78
	v_mul_f32_e32 v192, 0x3e0293ee, v79
	v_mul_f32_e32 v193, 0x3e0293ee, v80
	v_mul_f32_e32 v198, 0x3e0293ee, v81
	v_max_f32_e32 v170, 0, v171
	v_exp_f32_e64 v199, -|v171|
	v_max_f32_e32 v172, 0, v173
	v_exp_f32_e64 v200, -|v173|
	v_max_f32_e32 v178, 0, v179
	v_exp_f32_e64 v201, -|v179|
	v_max_f32_e32 v180, 0, v181
	v_exp_f32_e64 v202, -|v181|
	v_max_f32_e32 v171, 0, v182
	v_exp_f32_e64 v203, -|v182|
	v_max_f32_e32 v173, 0, v183
	v_exp_f32_e64 v204, -|v183|
	v_max_f32_e32 v179, 0, v184
	v_exp_f32_e64 v205, -|v184|
	v_max_f32_e32 v181, 0, v185
	v_exp_f32_e64 v206, -|v185|
	v_max_f32_e32 v183, 0, v186
	v_exp_f32_e64 v207, -|v186|
	v_max_f32_e32 v185, 0, v187
	v_exp_f32_e64 v208, -|v187|
	v_max_f32_e32 v187, 0, v188
	v_exp_f32_e64 v209, -|v188|
	v_max_f32_e32 v189, 0, v190
	v_exp_f32_e64 v190, -|v190|
	v_max_f32_e32 v182, 0, v191
	v_exp_f32_e64 v191, -|v191|
	v_max_f32_e32 v184, 0, v192
	v_exp_f32_e64 v192, -|v192|
	v_max_f32_e32 v186, 0, v193
	v_exp_f32_e64 v193, -|v193|
	v_max_f32_e32 v188, 0, v198
	v_exp_f32_e64 v198, -|v198|
	v_add_f32_e32 v199, 1.0, v199
	v_add_f32_e32 v200, 1.0, v200
	v_add_f32_e32 v201, 1.0, v201
	v_add_f32_e32 v202, 1.0, v202
	v_add_f32_e32 v203, 1.0, v203
	v_add_f32_e32 v204, 1.0, v204
	v_add_f32_e32 v205, 1.0, v205
	v_add_f32_e32 v206, 1.0, v206
	v_add_f32_e32 v207, 1.0, v207
	v_add_f32_e32 v208, 1.0, v208
	v_add_f32_e32 v209, 1.0, v209
	v_add_f32_e32 v225, 1.0, v190
	v_add_f32_e32 v226, 1.0, v191
	v_add_f32_e32 v227, 1.0, v192
	v_add_f32_e32 v228, 1.0, v193
	v_add_f32_e32 v229, 1.0, v198
	v_log_f32_e32 v190, v199
	v_log_f32_e32 v192, v200
	v_log_f32_e32 v198, v201
	v_log_f32_e32 v200, v202
	v_log_f32_e32 v191, v203
	v_log_f32_e32 v193, v204
	v_log_f32_e32 v199, v205
	v_log_f32_e32 v201, v206
	v_log_f32_e32 v203, v207
	v_log_f32_e32 v205, v208
	v_log_f32_e32 v207, v209
	v_log_f32_e32 v209, v225
	v_log_f32_e32 v202, v226
	v_log_f32_e32 v204, v227
	v_log_f32_e32 v206, v228
	v_log_f32_e32 v208, v229
	v_pk_add_f32 v[182:183], v[182:183], v[202:203]
	v_pk_add_f32 v[184:185], v[184:185], v[204:205]
	v_pk_add_f32 v[186:187], v[186:187], v[206:207]
	v_pk_add_f32 v[188:189], v[188:189], v[208:209]
	v_pk_add_f32 v[178:179], v[178:179], v[198:199]
	v_pk_add_f32 v[180:181], v[180:181], v[200:201]
	v_pk_add_f32 v[170:171], v[170:171], v[190:191]
	v_pk_add_f32 v[172:173], v[172:173], v[192:193]
	v_fma_f32 v190, v74, s38, -v183
	v_fma_f32 v192, v76, s38, -v187
	v_fma_f32 v193, v77, s38, -v189
	v_fma_f32 v198, v78, s38, -v182
	v_fma_f32 v199, v79, s38, -v184
	v_fma_f32 v200, v80, s38, -v186
	v_fma_f32 v201, v81, s38, -v188
	v_fma_f32 v205, v69, s38, -v180
	v_fma_f32 v208, v72, s38, -v179
	v_cndmask_b32_e64 v74, 0, -v180, s[12:13]
	v_fma_f32 v180, v73, s38, -v181
	v_cndmask_b32_e64 v73, 0, -v183, vcc
	v_cndmask_b32_e64 v72, 0, -v182, s[14:15]
	v_cndmask_b32_e64 v77, 0, -v185, s[24:25]
	v_cndmask_b32_e64 v76, 0, -v184, s[22:23]
	v_cndmask_b32_e64 v79, 0, -v187, s[28:29]
	v_cndmask_b32_e64 v78, 0, -v186, s[26:27]
	v_cndmask_b32_e64 v81, 0, -v189, s[34:35]
	v_cndmask_b32_e64 v80, 0, -v188, s[30:31]
	v_fma_f32 v191, v75, s38, -v185
	v_fma_f32 v202, v66, s38, -v170
	v_fma_f32 v203, v67, s38, -v172
	v_fma_f32 v204, v68, s38, -v178
	v_cndmask_b32_e64 v67, 0, -v171, s[6:7]
	v_cndmask_b32_e64 v66, 0, -v170, s[4:5]
	v_fma_f32 v206, v70, s38, -v171
	v_cndmask_b32_e64 v69, 0, -v173, s[16:17]
	v_cndmask_b32_e64 v68, 0, -v172, s[8:9]
	v_fma_f32 v207, v71, s38, -v173
	v_cndmask_b32_e64 v71, 0, -v179, s[18:19]
	v_cndmask_b32_e64 v70, 0, -v178, s[10:11]
	v_cndmask_b32_e64 v75, 0, -v181, s[20:21]
	v_pk_add_f32 v[72:73], v[72:73], v[76:77]
	v_pk_add_f32 v[172:173], v[78:79], v[80:81]
	v_pk_add_f32 v[66:67], v[66:67], v[68:69]
	v_pk_add_f32 v[170:171], v[70:71], v[74:75]
	v_pk_add_f32 v[72:73], v[72:73], v[172:173]
	v_pk_add_f32 v[66:67], v[66:67], v[170:171]
	ds_bpermute_b32 v173, v143, v73
	ds_bpermute_b32 v172, v143, v72
	ds_bpermute_b32 v170, v143, v66
	ds_bpermute_b32 v171, v143, v67
	v_cmp_lt_i32_e64 s[20:21], v169, v145
	v_cmp_lt_i32_e64 s[22:23], v169, v148
	s_waitcnt lgkmcnt(2)
	v_pk_add_f32 v[72:73], v[72:73], v[172:173]
	v_cmp_lt_i32_e64 s[24:25], v169, v160
	s_waitcnt lgkmcnt(0)
	v_pk_add_f32 v[178:179], v[66:67], v[170:171]
	v_cndmask_b32_e64 v67, 0, v171, s[0:1]
	v_cndmask_b32_e64 v171, 0, v172, s[0:1]
	v_add_f32_e32 v172, 0, v72
	v_cndmask_b32_e64 v66, 0, v170, s[0:1]
	v_cndmask_b32_e64 v170, 0, v173, s[0:1]
	v_add_f32_e32 v171, v197, v171
	v_add_f32_e32 v173, v73, v172
	v_add_f32_e32 v172, v149, v172
	v_add_f32_e32 v181, v171, v201
	v_add_f32_e32 v80, v171, v80
	v_add_f32_e32 v171, v179, v173
	v_add_f32_e32 v173, v149, v173
	v_add_f32_e32 v170, v170, v172
	v_exp_f32_e32 v172, v181
	v_add_f32_e32 v181, v200, v80
	v_add_f32_e32 v78, v78, v80
	v_add_f32_e32 v80, v149, v171
	v_add_f32_e32 v67, v67, v173
	v_add_f32_e32 v173, v199, v78
	v_add_f32_e32 v76, v76, v78
	v_add_f32_e32 v66, v66, v80
	v_add_f32_e32 v78, v180, v67
	v_add_f32_e32 v67, v75, v67
	v_add_f32_e32 v75, v205, v66
	v_add_f32_e32 v66, v74, v66
	v_exp_f32_e32 v74, v78
	v_add_f32_e32 v78, v208, v67
	v_add_f32_e32 v67, v71, v67
	v_exp_f32_e32 v71, v75
	v_add_f32_e32 v75, v204, v66
	v_add_f32_e32 v66, v70, v66
	v_exp_f32_e32 v70, v78
	v_add_f32_e32 v78, v207, v67
	v_add_f32_e32 v67, v69, v67
	v_exp_f32_e32 v69, v75
	v_add_f32_e32 v75, v203, v66
	v_add_f32_e32 v66, v68, v66
	v_add_f32_e32 v67, v206, v67
	v_exp_f32_e32 v68, v78
	v_add_f32_e32 v66, v202, v66
	v_exp_f32_e32 v67, v67
	v_exp_f32_e32 v75, v75
	v_exp_f32_e32 v66, v66
	v_cndmask_b32_e64 v74, 0, v74, s[20:21]
	v_cndmask_b32_e64 v70, 0, v70, s[22:23]
	v_add_f32_e32 v81, v81, v170
	v_cndmask_b32_e64 v71, 0, v71, s[12:13]
	v_cndmask_b32_e64 v78, 0, v69, s[10:11]
	v_cndmask_b32_e64 v68, 0, v68, s[24:25]
	v_cvt_pk_bf16_f32 v69, v70, v74
	v_cndmask_b32_e64 v74, 0, v67, s[6:7]
	v_cndmask_b32_e64 v70, 0, v75, s[8:9]
	v_cvt_pk_bf16_f32 v67, v78, v71
	v_cndmask_b32_e64 v66, 0, v66, s[4:5]
	v_cvt_pk_bf16_f32 v68, v74, v68
	v_add_f32_e32 v71, v192, v81
	v_add_f32_e32 v74, v79, v81
	v_add_f32_e32 v171, v193, v170
	v_cvt_pk_bf16_f32 v66, v66, v70
	v_exp_f32_e32 v78, v71
	v_add_f32_e32 v71, v191, v74
	v_add_f32_e32 v74, v77, v74
	v_mfma_f32_32x32x16_bf16 v[50:65], v[126:129], v[66:69], v[50:65]
	v_exp_f32_e32 v70, v171
	v_exp_f32_e32 v77, v71
	v_add_f32_e32 v71, v190, v74
	v_add_f32_e32 v76, v198, v76
	v_exp_f32_e32 v79, v71
	v_exp_f32_e32 v170, v181
	v_exp_f32_e32 v75, v173
	v_mfma_f32_32x32x16_bf16 v[34:49], v[130:133], v[66:69], v[34:49]
	v_exp_f32_e32 v76, v76
	v_cmp_lt_i32_e64 s[4:5], v169, v161
	v_cmp_lt_i32_e64 s[8:9], v169, v162
	v_cmp_lt_i32_e64 s[10:11], v169, v163
	v_cndmask_b32_e64 v70, 0, v70, s[4:5]
	v_cmp_lt_i32_e64 s[16:17], v169, v164
	v_cmp_lt_i32_e64 s[18:19], v169, v165
	s_waitcnt vmcnt(6)
	v_mfma_f32_32x32x16_bf16 v[18:33], v[114:117], v[66:69], v[18:33]
	v_cmp_lt_i32_e64 s[6:7], v169, v168
	v_cndmask_b32_e64 v74, 0, v172, s[16:17]
	v_cndmask_b32_e64 v71, 0, v170, s[18:19]
	v_cndmask_b32_e64 v75, 0, v75, s[6:7]
	v_cvt_pk_bf16_f32 v71, v71, v74
	s_waitcnt vmcnt(2)
	v_mfma_f32_32x32x16_bf16 v[2:17], v[174:177], v[66:69], v[2:17]
	v_cndmask_b32_e64 v66, 0, v78, s[8:9]
	v_cndmask_b32_e64 v68, 0, v77, s[10:11]
	v_cvt_pk_bf16_f32 v69, v66, v70
	v_cndmask_b32_e32 v66, 0, v79, vcc
	v_cndmask_b32_e64 v67, 0, v76, s[14:15]
	v_cvt_pk_bf16_f32 v68, v66, v68
	v_add_f32_e32 v66, v178, v179
	v_cvt_pk_bf16_f32 v70, v67, v75
	v_add_f32_e32 v66, v73, v66
	v_add_f32_e32 v66, v72, v66
	v_mfma_f32_32x32x16_bf16 v[50:65], v[118:121], v[68:71], v[50:65]
	v_add_f32_e32 v149, v149, v66
	v_cmp_gt_f32_e32 vcc, s39, v149
	s_cmp_lg_u64 vcc, exec
	s_cselect_b64 s[4:5], -1, 0
	s_cmp_lg_u32 s40, 0
	s_cselect_b64 s[6:7], -1, 0
	s_and_b64 s[4:5], s[6:7], s[4:5]
	v_mfma_f32_32x32x16_bf16 v[34:49], v[122:125], v[68:71], v[34:49]
	s_sub_i32 s40, s40, 32
	s_and_b64 vcc, exec, s[4:5]
	v_mfma_f32_32x32x16_bf16 v[18:33], v[138:141], v[68:71], v[18:33]
	s_waitcnt vmcnt(0)
	v_mfma_f32_32x32x16_bf16 v[2:17], v[134:137], v[68:71], v[2:17]
	s_cbranch_vccnz .LBB0_303
	v_mul_f32_e32 v84, v51, v51
	v_fmac_f32_e32 v84, v50, v50
	v_fmac_f32_e32 v84, v52, v52
	v_fmac_f32_e32 v84, v53, v53
	v_fmac_f32_e32 v84, v54, v54
	v_fmac_f32_e32 v84, v55, v55
	v_fmac_f32_e32 v84, v56, v56
	v_fmac_f32_e32 v84, v57, v57
	v_fmac_f32_e32 v84, v58, v58
	v_fmac_f32_e32 v84, v59, v59
	v_fmac_f32_e32 v84, v60, v60
	v_fmac_f32_e32 v84, v61, v61
	v_fmac_f32_e32 v84, v62, v62
	v_fmac_f32_e32 v84, v63, v63
	v_fmac_f32_e32 v84, v64, v64
	v_fmac_f32_e32 v84, v65, v65
	v_fmac_f32_e32 v84, v34, v34
	v_fmac_f32_e32 v84, v35, v35
	v_fmac_f32_e32 v84, v36, v36
	v_fmac_f32_e32 v84, v37, v37
	v_fmac_f32_e32 v84, v38, v38
	v_fmac_f32_e32 v84, v39, v39
	v_fmac_f32_e32 v84, v40, v40
	v_fmac_f32_e32 v84, v41, v41
	v_fmac_f32_e32 v84, v42, v42
	v_fmac_f32_e32 v84, v43, v43
	v_fmac_f32_e32 v84, v44, v44
	v_fmac_f32_e32 v84, v45, v45
	v_fmac_f32_e32 v84, v46, v46
	v_fmac_f32_e32 v84, v47, v47
	v_fmac_f32_e32 v84, v48, v48
	v_fmac_f32_e32 v84, v49, v49
	v_fmac_f32_e32 v84, v18, v18
	v_fmac_f32_e32 v84, v19, v19
	v_fmac_f32_e32 v84, v20, v20
	v_fmac_f32_e32 v84, v21, v21
	v_fmac_f32_e32 v84, v22, v22
	v_fmac_f32_e32 v84, v23, v23
	v_fmac_f32_e32 v84, v24, v24
	v_fmac_f32_e32 v84, v25, v25
	v_fmac_f32_e32 v84, v26, v26
	v_fmac_f32_e32 v84, v27, v27
	v_fmac_f32_e32 v84, v28, v28
	v_fmac_f32_e32 v84, v29, v29
	v_fmac_f32_e32 v84, v30, v30
	v_fmac_f32_e32 v84, v31, v31
	v_fmac_f32_e32 v84, v32, v32
	v_fmac_f32_e32 v84, v33, v33
	v_fmac_f32_e32 v84, v2, v2
	v_fmac_f32_e32 v84, v3, v3
	s_lshl_b32 s0, s33, 2
	v_fmac_f32_e32 v84, v4, v4
	s_add_u32 s4, s60, s0
	v_fmac_f32_e32 v84, v5, v5
	s_addc_u32 s5, s61, 0
	v_lshlrev_b32_e32 v1, 2, v166
	v_fmac_f32_e32 v84, v6, v6
	global_load_dwordx4 v[66:69], v1, s[4:5]
	global_load_dwordx4 v[70:73], v1, s[4:5] offset:32
	v_fmac_f32_e32 v84, v7, v7
	v_fmac_f32_e32 v84, v8, v8
	v_fmac_f32_e32 v84, v9, v9
	v_fmac_f32_e32 v84, v10, v10
	v_fmac_f32_e32 v84, v11, v11
	v_pk_mul_f32 v[82:83], v[12:13], v[12:13]
	v_pk_mul_f32 v[80:81], v[14:15], v[14:15]
	v_add_f32_e32 v82, v82, v84
	global_load_dwordx4 v[74:77], v1, s[4:5] offset:64
	v_add_f32_e32 v82, v83, v82
	v_add_f32_e32 v80, v80, v82
	v_pk_mul_f32 v[78:79], v[16:17], v[16:17]
	v_add_f32_e32 v80, v81, v80
	v_add_f32_e32 v78, v78, v80
	v_add_f32_e32 v82, v79, v78
	global_load_dwordx4 v[78:81], v1, s[4:5] offset:96
	ds_bpermute_b32 v83, v143, v82
	v_mov_b32_e32 v87, 0x358637bd
	s_mov_b32 s0, 0xf800000
	v_or_b32_e32 v90, s42, v142
	v_ashrrev_i32_e32 v91, 31, v90
	s_waitcnt lgkmcnt(0)
	v_add_f32_e32 v86, v82, v83
	v_fmac_f32_e32 v87, 0x3c000000, v86
	v_mul_f32_e32 v86, 0x4f800000, v87
	v_cmp_gt_f32_e32 vcc, s0, v87
	v_lshlrev_b64 v[90:91], 12, v[90:91]
	s_mov_b32 s7, 0
	v_cndmask_b32_e32 v98, v87, v86, vcc
	v_sqrt_f32_e32 v94, v98
	v_lshl_add_u64 v[102:103], s[2:3], 0, v[90:91]
	s_lshl_b32 s6, s33, 1
	v_lshl_add_u64 v[102:103], v[102:103], 0, s[6:7]
	v_add_u32_e32 v95, -1, v94
	v_fma_f32 v96, -v95, v94, v98
	v_cmp_ge_f32_e64 s[0:1], 0, v96
	v_add_u32_e32 v96, 1, v94
	v_mov_b32_e32 v145, 0
	v_cndmask_b32_e64 v95, v94, v95, s[0:1]
	v_fma_f32 v94, -v96, v94, v98
	v_cmp_lt_f32_e64 s[0:1], 0, v94
	v_lshl_add_u64 v[110:111], v[102:103], 0, v[144:145]
	global_load_dwordx4 v[82:85], v1, s[4:5] offset:128
	global_load_dwordx4 v[86:89], v1, s[4:5] offset:160
	v_cndmask_b32_e64 v99, v95, v96, s[0:1]
	v_mul_f32_e32 v100, 0x37800000, v99
	v_cndmask_b32_e32 v99, v99, v100, vcc
	v_mov_b32_e32 v100, 0x260
	v_cmp_class_f32_e32 vcc, v98, v100
	global_load_dwordx4 v[90:93], v1, s[4:5] offset:192
	global_load_dwordx4 v[94:97], v1, s[4:5] offset:224
	v_cndmask_b32_e32 v112, v99, v98, vcc
	v_div_scale_f32 v106, s[0:1], v112, v112, 1.0
	v_rcp_f32_e32 v113, v106
	v_div_scale_f32 v107, vcc, 1.0, v112, 1.0
	global_load_dwordx4 v[98:101], v1, s[4:5] offset:256
	v_fma_f32 v102, -v106, v113, 1.0
	v_fmac_f32_e32 v113, v102, v113
	v_mul_f32_e32 v114, v107, v113
	v_fma_f32 v108, -v106, v114, v107
	v_fmac_f32_e32 v114, v108, v113
	v_fma_f32 v115, -v106, v114, v107
	v_div_fmas_f32 v113, v115, v113, v114
	v_div_fixup_f32 v112, v113, v112, 1.0
	v_pk_mul_f32 v[50:51], v[50:51], v[112:113] op_sel_hi:[1,0]
	v_pk_mul_f32 v[114:115], v[52:53], v[112:113] op_sel_hi:[1,0]
	v_pk_mul_f32 v[54:55], v[54:55], v[112:113] op_sel_hi:[1,0]
	v_pk_mul_f32 v[56:57], v[56:57], v[112:113] op_sel_hi:[1,0]
	global_load_dwordx4 v[102:105], v1, s[4:5] offset:288
	v_pk_mul_f32 v[58:59], v[58:59], v[112:113] op_sel_hi:[1,0]
	v_pk_mul_f32 v[60:61], v[60:61], v[112:113] op_sel_hi:[1,0]
	global_load_dwordx4 v[106:109], v1, s[4:5] offset:320
	v_pk_mul_f32 v[62:63], v[62:63], v[112:113] op_sel_hi:[1,0]
	v_pk_mul_f32 v[64:65], v[64:65], v[112:113] op_sel_hi:[1,0]
	v_pk_mul_f32 v[34:35], v[34:35], v[112:113] op_sel_hi:[1,0]
	v_pk_mul_f32 v[36:37], v[36:37], v[112:113] op_sel_hi:[1,0]
	v_pk_mul_f32 v[18:19], v[18:19], v[112:113] op_sel_hi:[1,0]
	s_waitcnt vmcnt(10)
	v_pk_mul_f32 v[66:67], v[66:67], v[50:51]
	v_pk_mul_f32 v[68:69], v[68:69], v[114:115]
	v_cvt_pk_bf16_f32 v66, v66, v67
	v_cvt_pk_bf16_f32 v67, v68, v69
	global_store_dwordx2 v[110:111], v[66:67], off
	global_load_dwordx4 v[66:69], v1, s[4:5] offset:384
	s_waitcnt vmcnt(11)
	v_pk_mul_f32 v[54:55], v[70:71], v[54:55]
	v_pk_mul_f32 v[56:57], v[72:73], v[56:57]
	v_cvt_pk_bf16_f32 v54, v54, v55
	v_cvt_pk_bf16_f32 v55, v56, v57
	global_store_dwordx2 v[110:111], v[54:55], off offset:16
	global_load_dwordx4 v[54:57], v1, s[4:5] offset:416
	s_waitcnt vmcnt(12)
	v_pk_mul_f32 v[58:59], v[74:75], v[58:59]
	v_pk_mul_f32 v[60:61], v[76:77], v[60:61]
	v_cvt_pk_bf16_f32 v58, v58, v59
	v_cvt_pk_bf16_f32 v59, v60, v61
	global_store_dwordx2 v[110:111], v[58:59], off offset:32
	global_load_dwordx4 v[58:61], v1, s[4:5] offset:448
	s_waitcnt vmcnt(13)
	v_pk_mul_f32 v[62:63], v[62:63], v[78:79]
	v_pk_mul_f32 v[64:65], v[64:65], v[80:81]
	global_load_dwordx4 v[50:53], v1, s[4:5] offset:352
	v_cvt_pk_bf16_f32 v70, v62, v63
	v_cvt_pk_bf16_f32 v71, v64, v65
	global_load_dwordx4 v[62:65], v1, s[4:5] offset:480
	v_pk_mul_f32 v[20:21], v[20:21], v[112:113] op_sel_hi:[1,0]
	v_pk_mul_f32 v[2:3], v[2:3], v[112:113] op_sel_hi:[1,0]
	v_pk_mul_f32 v[4:5], v[4:5], v[112:113] op_sel_hi:[1,0]
	global_store_dwordx2 v[110:111], v[70:71], off offset:48
	s_waitcnt vmcnt(15)
	v_pk_mul_f32 v[34:35], v[34:35], v[82:83]
	v_pk_mul_f32 v[36:37], v[36:37], v[84:85]
	v_cvt_pk_bf16_f32 v34, v34, v35
	v_cvt_pk_bf16_f32 v35, v36, v37
	global_store_dwordx2 v[110:111], v[34:35], off offset:64
	v_pk_mul_f32 v[34:35], v[38:39], v[112:113] op_sel_hi:[1,0]
	v_pk_mul_f32 v[36:37], v[40:41], v[112:113] op_sel_hi:[1,0]
	s_waitcnt vmcnt(15)
	v_pk_mul_f32 v[34:35], v[34:35], v[86:87]
	v_pk_mul_f32 v[36:37], v[36:37], v[88:89]
	v_cvt_pk_bf16_f32 v34, v34, v35
	v_cvt_pk_bf16_f32 v35, v36, v37
	global_store_dwordx2 v[110:111], v[34:35], off offset:80
	v_pk_mul_f32 v[34:35], v[42:43], v[112:113] op_sel_hi:[1,0]
	v_pk_mul_f32 v[36:37], v[44:45], v[112:113] op_sel_hi:[1,0]
	s_waitcnt vmcnt(15)
	v_pk_mul_f32 v[34:35], v[34:35], v[90:91]
	s_waitcnt vmcnt(13)
	v_pk_mul_f32 v[18:19], v[18:19], v[98:99]
	v_pk_mul_f32 v[20:21], v[20:21], v[100:101]
	v_cvt_pk_bf16_f32 v18, v18, v19
	v_cvt_pk_bf16_f32 v19, v20, v21
	global_store_dwordx2 v[110:111], v[18:19], off offset:128
	v_pk_mul_f32 v[18:19], v[22:23], v[112:113] op_sel_hi:[1,0]
	v_pk_mul_f32 v[20:21], v[24:25], v[112:113] op_sel_hi:[1,0]
	v_pk_mul_f32 v[36:37], v[36:37], v[92:93]
	v_cvt_pk_bf16_f32 v34, v34, v35
	v_cvt_pk_bf16_f32 v35, v36, v37
	global_store_dwordx2 v[110:111], v[34:35], off offset:96
	v_pk_mul_f32 v[34:35], v[46:47], v[112:113] op_sel_hi:[1,0]
	v_pk_mul_f32 v[36:37], v[48:49], v[112:113] op_sel_hi:[1,0]
	s_waitcnt vmcnt(14)
	v_pk_mul_f32 v[18:19], v[18:19], v[102:103]
	v_pk_mul_f32 v[20:21], v[20:21], v[104:105]
	v_cvt_pk_bf16_f32 v18, v18, v19
	v_cvt_pk_bf16_f32 v19, v20, v21
	global_store_dwordx2 v[110:111], v[18:19], off offset:144
	v_pk_mul_f32 v[18:19], v[26:27], v[112:113] op_sel_hi:[1,0]
	v_pk_mul_f32 v[20:21], v[28:29], v[112:113] op_sel_hi:[1,0]
	s_waitcnt vmcnt(14)
	v_pk_mul_f32 v[18:19], v[18:19], v[106:107]
	v_pk_mul_f32 v[20:21], v[20:21], v[108:109]
	v_cvt_pk_bf16_f32 v18, v18, v19
	v_cvt_pk_bf16_f32 v19, v20, v21
	global_store_dwordx2 v[110:111], v[18:19], off offset:160
	v_pk_mul_f32 v[18:19], v[30:31], v[112:113] op_sel_hi:[1,0]
	v_pk_mul_f32 v[20:21], v[32:33], v[112:113] op_sel_hi:[1,0]
	s_waitcnt vmcnt(13)
	v_pk_mul_f32 v[2:3], v[2:3], v[66:67]
	v_pk_mul_f32 v[4:5], v[4:5], v[68:69]
	v_cvt_pk_bf16_f32 v2, v2, v3
	v_cvt_pk_bf16_f32 v3, v4, v5
	global_store_dwordx2 v[110:111], v[2:3], off offset:192
	v_pk_mul_f32 v[2:3], v[6:7], v[112:113] op_sel_hi:[1,0]
	v_pk_mul_f32 v[4:5], v[8:9], v[112:113] op_sel_hi:[1,0]
	s_waitcnt vmcnt(12)
	v_pk_mul_f32 v[2:3], v[2:3], v[54:55]
	v_pk_mul_f32 v[4:5], v[4:5], v[56:57]
	v_cvt_pk_bf16_f32 v2, v2, v3
	v_cvt_pk_bf16_f32 v3, v4, v5
	global_store_dwordx2 v[110:111], v[2:3], off offset:208
	v_pk_mul_f32 v[2:3], v[10:11], v[112:113] op_sel_hi:[1,0]
	v_pk_mul_f32 v[4:5], v[12:13], v[112:113] op_sel_hi:[1,0]
	s_waitcnt vmcnt(11)
	v_pk_mul_f32 v[2:3], v[2:3], v[58:59]
	v_pk_mul_f32 v[4:5], v[4:5], v[60:61]
	v_cvt_pk_bf16_f32 v2, v2, v3
	v_cvt_pk_bf16_f32 v3, v4, v5
	global_store_dwordx2 v[110:111], v[2:3], off offset:224
	v_pk_mul_f32 v[2:3], v[14:15], v[112:113] op_sel_hi:[1,0]
	v_pk_mul_f32 v[4:5], v[16:17], v[112:113] op_sel_hi:[1,0]
	v_pk_mul_f32 v[34:35], v[34:35], v[94:95]
	v_pk_mul_f32 v[36:37], v[36:37], v[96:97]
	s_waitcnt vmcnt(11)
	v_pk_mul_f32 v[18:19], v[18:19], v[50:51]
	v_pk_mul_f32 v[20:21], v[20:21], v[52:53]
	s_waitcnt vmcnt(10)
	v_pk_mul_f32 v[2:3], v[2:3], v[62:63]
	v_pk_mul_f32 v[4:5], v[4:5], v[64:65]
	v_cvt_pk_bf16_f32 v34, v34, v35
	v_cvt_pk_bf16_f32 v35, v36, v37
	v_cvt_pk_bf16_f32 v18, v18, v19
	v_cvt_pk_bf16_f32 v19, v20, v21
	v_cvt_pk_bf16_f32 v2, v2, v3
	v_cvt_pk_bf16_f32 v3, v4, v5
	global_store_dwordx2 v[110:111], v[34:35], off offset:112
	global_store_dwordx2 v[110:111], v[18:19], off offset:176
	global_store_dwordx2 v[110:111], v[2:3], off offset:240

.LBB0_359:
	s_add_u32 s14, s94, 0x3f5d0000
	s_addc_u32 s15, s95, 0
	s_add_u32 s16, s94, 0x43610000
	s_addc_u32 s17, s95, 0
	s_add_u32 s18, s94, 0x435d0000
	s_addc_u32 s19, s95, 0
	global_load_dwordx2 v[242:243], v4, s[14:15]
	global_load_dwordx4 v[198:201], v2, s[18:19]
	s_add_u32 s14, s14, 0x10000
	s_addc_u32 s15, s15, 0
	s_add_u32 s18, s18, 0x200
	s_addc_u32 s19, s19, 0
	global_load_dwordx2 v[244:245], v4, s[14:15]
	global_load_dwordx4 v[202:205], v2, s[18:19]
	s_add_u32 s14, s14, 0x10000
	s_addc_u32 s15, s15, 0
	s_add_u32 s18, s18, 0x200
	s_addc_u32 s19, s19, 0
	global_load_dwordx2 v[246:247], v4, s[14:15]
	global_load_dwordx4 v[206:209], v2, s[18:19]
	s_add_u32 s14, s14, 0x10000
	s_addc_u32 s15, s15, 0
	s_add_u32 s18, s18, 0x200
	s_addc_u32 s19, s19, 0
	global_load_dwordx2 v[248:249], v4, s[14:15]
	global_load_dwordx4 v[218:221], v2, s[18:19]
	s_add_u32 s14, s14, 0x10000
	s_addc_u32 s15, s15, 0
	s_add_u32 s18, s18, 0x200
	s_addc_u32 s19, s19, 0
	global_load_dwordx2 v[250:251], v4, s[14:15]
	global_load_dwordx4 v[222:225], v2, s[18:19]
	s_add_u32 s14, s14, 0x10000
	s_addc_u32 s15, s15, 0
	s_add_u32 s18, s18, 0x200
	s_addc_u32 s19, s19, 0
	global_load_dwordx2 v[252:253], v4, s[14:15]
	global_load_dwordx4 v[226:229], v2, s[18:19]
	s_add_u32 s14, s14, 0x10000
	s_addc_u32 s15, s15, 0
	s_add_u32 s18, s18, 0x200
	s_addc_u32 s19, s19, 0
	global_load_dwordx2 v[212:213], v4, s[14:15]
	global_load_dwordx4 v[230:233], v2, s[18:19]
	s_add_u32 s14, s14, 0x10000
	s_addc_u32 s15, s15, 0
	s_add_u32 s18, s18, 0x200
	s_addc_u32 s19, s19, 0
	global_load_dwordx2 v[234:235], v4, s[14:15]
	global_load_dwordx4 v[238:241], v2, s[18:19]
	s_add_u32 s14, s14, 0x10000
	s_addc_u32 s15, s15, 0
	s_add_u32 s18, s18, 0x200
	s_addc_u32 s19, s19, 0
	v_cvt_pk_bf16_f32 v6, v10, v11
	v_cvt_pk_bf16_f32 v7, v12, v13
	global_store_dwordx2 v4, v[6:7], s[16:17]
	s_add_u32 s16, s16, 0x10000
	s_addc_u32 s17, s17, 0
	s_waitcnt vmcnt(15)
	v_lshlrev_b32_e32 v16, 16, v242
	v_and_b32_e32 v17, 0xffff0000, v242
	v_lshlrev_b32_e32 v18, 16, v243
	v_and_b32_e32 v19, 0xffff0000, v243
	v_pk_fma_f32 v[10:11], v[10:11], v[198:199], v[16:17]
	v_pk_fma_f32 v[12:13], v[12:13], v[200:201], v[18:19]
	global_load_dwordx2 v[242:243], v4, s[14:15]
	global_load_dwordx4 v[198:201], v2, s[18:19]
	s_add_u32 s14, s14, 0x10000
	s_addc_u32 s15, s15, 0
	s_add_u32 s18, s18, 0x200
	s_addc_u32 s19, s19, 0
	v_cvt_pk_bf16_f32 v8, v10, v11
	v_cvt_pk_bf16_f32 v9, v12, v13
	global_store_dwordx2 v4, v[8:9], s[16:17]
	s_add_u32 s16, s16, 0x10000
	s_addc_u32 s17, s17, 0
	s_waitcnt vmcnt(16)
	v_lshlrev_b32_e32 v16, 16, v244
	v_and_b32_e32 v17, 0xffff0000, v244
	v_lshlrev_b32_e32 v18, 16, v245
	v_and_b32_e32 v19, 0xffff0000, v245
	v_pk_fma_f32 v[10:11], v[10:11], v[202:203], v[16:17]
	v_pk_fma_f32 v[12:13], v[12:13], v[204:205], v[18:19]
	global_load_dwordx2 v[244:245], v4, s[14:15]
	global_load_dwordx4 v[202:205], v2, s[18:19]
	s_add_u32 s14, s14, 0x10000
	s_addc_u32 s15, s15, 0
	s_add_u32 s18, s18, 0x200
	s_addc_u32 s19, s19, 0
	v_cvt_pk_bf16_f32 v6, v10, v11
	v_cvt_pk_bf16_f32 v7, v12, v13
	global_store_dwordx2 v4, v[6:7], s[16:17]
	s_add_u32 s16, s16, 0x10000
	s_addc_u32 s17, s17, 0
	s_waitcnt vmcnt(17)
	v_lshlrev_b32_e32 v16, 16, v246
	v_and_b32_e32 v17, 0xffff0000, v246
	v_lshlrev_b32_e32 v18, 16, v247
	v_and_b32_e32 v19, 0xffff0000, v247
	v_pk_fma_f32 v[10:11], v[10:11], v[206:207], v[16:17]
	v_pk_fma_f32 v[12:13], v[12:13], v[208:209], v[18:19]
	global_load_dwordx2 v[246:247], v4, s[14:15]
	global_load_dwordx4 v[206:209], v2, s[18:19]
	s_add_u32 s14, s14, 0x10000
	s_addc_u32 s15, s15, 0
	s_add_u32 s18, s18, 0x200
	s_addc_u32 s19, s19, 0
	v_cvt_pk_bf16_f32 v8, v10, v11
	v_cvt_pk_bf16_f32 v9, v12, v13
	global_store_dwordx2 v4, v[8:9], s[16:17]
	s_add_u32 s16, s16, 0x10000
	s_addc_u32 s17, s17, 0
	s_waitcnt vmcnt(18)
	v_lshlrev_b32_e32 v16, 16, v248
	v_and_b32_e32 v17, 0xffff0000, v248
	v_lshlrev_b32_e32 v18, 16, v249
	v_and_b32_e32 v19, 0xffff0000, v249
	v_pk_fma_f32 v[10:11], v[10:11], v[218:219], v[16:17]
	v_pk_fma_f32 v[12:13], v[12:13], v[220:221], v[18:19]
	global_load_dwordx2 v[248:249], v4, s[14:15]
	global_load_dwordx4 v[218:221], v2, s[18:19]
	s_add_u32 s14, s14, 0x10000
	s_addc_u32 s15, s15, 0
	s_add_u32 s18, s18, 0x200
	s_addc_u32 s19, s19, 0
	v_cvt_pk_bf16_f32 v6, v10, v11
	v_cvt_pk_bf16_f32 v7, v12, v13
	global_store_dwordx2 v4, v[6:7], s[16:17]
	s_add_u32 s16, s16, 0x10000
	s_addc_u32 s17, s17, 0
	s_waitcnt vmcnt(19)
	v_lshlrev_b32_e32 v16, 16, v250
	v_and_b32_e32 v17, 0xffff0000, v250
	v_lshlrev_b32_e32 v18, 16, v251
	v_and_b32_e32 v19, 0xffff0000, v251
	v_pk_fma_f32 v[10:11], v[10:11], v[222:223], v[16:17]
	v_pk_fma_f32 v[12:13], v[12:13], v[224:225], v[18:19]
	global_load_dwordx2 v[250:251], v4, s[14:15]
	global_load_dwordx4 v[222:225], v2, s[18:19]
	s_add_u32 s14, s14, 0x10000
	s_addc_u32 s15, s15, 0
	s_add_u32 s18, s18, 0x200
	s_addc_u32 s19, s19, 0
	v_cvt_pk_bf16_f32 v8, v10, v11
	v_cvt_pk_bf16_f32 v9, v12, v13
	global_store_dwordx2 v4, v[8:9], s[16:17]
	s_add_u32 s16, s16, 0x10000
	s_addc_u32 s17, s17, 0
	s_waitcnt vmcnt(20)
	v_lshlrev_b32_e32 v16, 16, v252
	v_and_b32_e32 v17, 0xffff0000, v252
	v_lshlrev_b32_e32 v18, 16, v253
	v_and_b32_e32 v19, 0xffff0000, v253
	v_pk_fma_f32 v[10:11], v[10:11], v[226:227], v[16:17]
	v_pk_fma_f32 v[12:13], v[12:13], v[228:229], v[18:19]
	global_load_dwordx2 v[252:253], v4, s[14:15]
	global_load_dwordx4 v[226:229], v2, s[18:19]
	s_add_u32 s14, s14, 0x10000
	s_addc_u32 s15, s15, 0
	s_add_u32 s18, s18, 0x200
	s_addc_u32 s19, s19, 0
	v_cvt_pk_bf16_f32 v6, v10, v11
	v_cvt_pk_bf16_f32 v7, v12, v13
	global_store_dwordx2 v4, v[6:7], s[16:17]
	s_add_u32 s16, s16, 0x10000
	s_addc_u32 s17, s17, 0
	s_waitcnt vmcnt(21)
	v_lshlrev_b32_e32 v16, 16, v212
	v_and_b32_e32 v17, 0xffff0000, v212
	v_lshlrev_b32_e32 v18, 16, v213
	v_and_b32_e32 v19, 0xffff0000, v213
	v_pk_fma_f32 v[10:11], v[10:11], v[230:231], v[16:17]
	v_pk_fma_f32 v[12:13], v[12:13], v[232:233], v[18:19]
	global_load_dwordx2 v[212:213], v4, s[14:15]
	global_load_dwordx4 v[230:233], v2, s[18:19]
	s_add_u32 s14, s14, 0x10000
	s_addc_u32 s15, s15, 0
	s_add_u32 s18, s18, 0x200
	s_addc_u32 s19, s19, 0
	v_cvt_pk_bf16_f32 v8, v10, v11
	v_cvt_pk_bf16_f32 v9, v12, v13
	global_store_dwordx2 v4, v[8:9], s[16:17]
	s_add_u32 s16, s16, 0x10000
	s_addc_u32 s17, s17, 0
	s_waitcnt vmcnt(22)
	v_lshlrev_b32_e32 v16, 16, v234
	v_and_b32_e32 v17, 0xffff0000, v234
	v_lshlrev_b32_e32 v18, 16, v235
	v_and_b32_e32 v19, 0xffff0000, v235
	v_pk_fma_f32 v[10:11], v[10:11], v[238:239], v[16:17]
	v_pk_fma_f32 v[12:13], v[12:13], v[240:241], v[18:19]
	global_load_dwordx2 v[234:235], v4, s[14:15]
	global_load_dwordx4 v[238:241], v2, s[18:19]
	s_add_u32 s14, s14, 0x10000
	s_addc_u32 s15, s15, 0
	s_add_u32 s18, s18, 0x200
	s_addc_u32 s19, s19, 0
	v_cvt_pk_bf16_f32 v6, v10, v11
	v_cvt_pk_bf16_f32 v7, v12, v13
	global_store_dwordx2 v4, v[6:7], s[16:17]
	s_add_u32 s16, s16, 0x10000
	s_addc_u32 s17, s17, 0
	s_waitcnt vmcnt(22)
	v_lshlrev_b32_e32 v16, 16, v242
	v_and_b32_e32 v17, 0xffff0000, v242
	v_lshlrev_b32_e32 v18, 16, v243
	v_and_b32_e32 v19, 0xffff0000, v243
	v_pk_fma_f32 v[10:11], v[10:11], v[198:199], v[16:17]
	v_pk_fma_f32 v[12:13], v[12:13], v[200:201], v[18:19]
	global_load_dwordx2 v[242:243], v4, s[14:15]
	global_load_dwordx4 v[198:201], v2, s[18:19]
	s_add_u32 s14, s14, 0x10000
	s_addc_u32 s15, s15, 0
	s_add_u32 s18, s18, 0x200
	s_addc_u32 s19, s19, 0
	v_cvt_pk_bf16_f32 v8, v10, v11
	v_cvt_pk_bf16_f32 v9, v12, v13
	global_store_dwordx2 v4, v[8:9], s[16:17]
	s_add_u32 s16, s16, 0x10000
	s_addc_u32 s17, s17, 0
	s_waitcnt vmcnt(22)
	v_lshlrev_b32_e32 v16, 16, v244
	v_and_b32_e32 v17, 0xffff0000, v244
	v_lshlrev_b32_e32 v18, 16, v245
	v_and_b32_e32 v19, 0xffff0000, v245
	v_pk_fma_f32 v[10:11], v[10:11], v[202:203], v[16:17]
	v_pk_fma_f32 v[12:13], v[12:13], v[204:205], v[18:19]
	global_load_dwordx2 v[244:245], v4, s[14:15]
	global_load_dwordx4 v[202:205], v2, s[18:19]
	s_add_u32 s14, s14, 0x10000
	s_addc_u32 s15, s15, 0
	s_add_u32 s18, s18, 0x200
	s_addc_u32 s19, s19, 0
	v_cvt_pk_bf16_f32 v6, v10, v11
	v_cvt_pk_bf16_f32 v7, v12, v13
	global_store_dwordx2 v4, v[6:7], s[16:17]
	s_add_u32 s16, s16, 0x10000
	s_addc_u32 s17, s17, 0
	s_waitcnt vmcnt(22)
	v_lshlrev_b32_e32 v16, 16, v246
	v_and_b32_e32 v17, 0xffff0000, v246
	v_lshlrev_b32_e32 v18, 16, v247
	v_and_b32_e32 v19, 0xffff0000, v247
	v_pk_fma_f32 v[10:11], v[10:11], v[206:207], v[16:17]
	v_pk_fma_f32 v[12:13], v[12:13], v[208:209], v[18:19]
	global_load_dwordx2 v[246:247], v4, s[14:15]
	global_load_dwordx4 v[206:209], v2, s[18:19]
	s_add_u32 s14, s14, 0x10000
	s_addc_u32 s15, s15, 0
	s_add_u32 s18, s18, 0x200
	s_addc_u32 s19, s19, 0
	v_cvt_pk_bf16_f32 v8, v10, v11
	v_cvt_pk_bf16_f32 v9, v12, v13
	global_store_dwordx2 v4, v[8:9], s[16:17]
	s_add_u32 s16, s16, 0x10000
	s_addc_u32 s17, s17, 0
	s_waitcnt vmcnt(22)
	v_lshlrev_b32_e32 v16, 16, v248
	v_and_b32_e32 v17, 0xffff0000, v248
	v_lshlrev_b32_e32 v18, 16, v249
	v_and_b32_e32 v19, 0xffff0000, v249
	v_pk_fma_f32 v[10:11], v[10:11], v[218:219], v[16:17]
	v_pk_fma_f32 v[12:13], v[12:13], v[220:221], v[18:19]
	global_load_dwordx2 v[248:249], v4, s[14:15]
	global_load_dwordx4 v[218:221], v2, s[18:19]
	s_add_u32 s14, s14, 0x10000
	s_addc_u32 s15, s15, 0
	s_add_u32 s18, s18, 0x200
	s_addc_u32 s19, s19, 0
	v_cvt_pk_bf16_f32 v6, v10, v11
	v_cvt_pk_bf16_f32 v7, v12, v13
	global_store_dwordx2 v4, v[6:7], s[16:17]
	s_add_u32 s16, s16, 0x10000
	s_addc_u32 s17, s17, 0
	s_waitcnt vmcnt(22)
	v_lshlrev_b32_e32 v16, 16, v250
	v_and_b32_e32 v17, 0xffff0000, v250
	v_lshlrev_b32_e32 v18, 16, v251
	v_and_b32_e32 v19, 0xffff0000, v251
	v_pk_fma_f32 v[10:11], v[10:11], v[222:223], v[16:17]
	v_pk_fma_f32 v[12:13], v[12:13], v[224:225], v[18:19]
	global_load_dwordx2 v[250:251], v4, s[14:15]
	global_load_dwordx4 v[222:225], v2, s[18:19]
	s_add_u32 s14, s14, 0x10000
	s_addc_u32 s15, s15, 0
	s_add_u32 s18, s18, 0x200
	s_addc_u32 s19, s19, 0
	v_cvt_pk_bf16_f32 v8, v10, v11
	v_cvt_pk_bf16_f32 v9, v12, v13
	global_store_dwordx2 v4, v[8:9], s[16:17]
	s_add_u32 s16, s16, 0x10000
	s_addc_u32 s17, s17, 0
	s_waitcnt vmcnt(22)
	v_lshlrev_b32_e32 v16, 16, v252
	v_and_b32_e32 v17, 0xffff0000, v252
	v_lshlrev_b32_e32 v18, 16, v253
	v_and_b32_e32 v19, 0xffff0000, v253
	v_pk_fma_f32 v[10:11], v[10:11], v[226:227], v[16:17]
	v_pk_fma_f32 v[12:13], v[12:13], v[228:229], v[18:19]
	global_load_dwordx2 v[252:253], v4, s[14:15]
	global_load_dwordx4 v[226:229], v2, s[18:19]
	s_add_u32 s14, s14, 0x10000
	s_addc_u32 s15, s15, 0
	s_add_u32 s18, s18, 0x200
	s_addc_u32 s19, s19, 0
	v_cvt_pk_bf16_f32 v6, v10, v11
	v_cvt_pk_bf16_f32 v7, v12, v13
	global_store_dwordx2 v4, v[6:7], s[16:17]
	s_add_u32 s16, s16, 0x10000
	s_addc_u32 s17, s17, 0
	s_waitcnt vmcnt(22)
	v_lshlrev_b32_e32 v16, 16, v212
	v_and_b32_e32 v17, 0xffff0000, v212
	v_lshlrev_b32_e32 v18, 16, v213
	v_and_b32_e32 v19, 0xffff0000, v213
	v_pk_fma_f32 v[10:11], v[10:11], v[230:231], v[16:17]
	v_pk_fma_f32 v[12:13], v[12:13], v[232:233], v[18:19]
	global_load_dwordx2 v[212:213], v4, s[14:15]
	global_load_dwordx4 v[230:233], v2, s[18:19]
	s_add_u32 s14, s14, 0x10000
	s_addc_u32 s15, s15, 0
	s_add_u32 s18, s18, 0x200
	s_addc_u32 s19, s19, 0
	v_cvt_pk_bf16_f32 v8, v10, v11
	v_cvt_pk_bf16_f32 v9, v12, v13
	global_store_dwordx2 v4, v[8:9], s[16:17]
	s_add_u32 s16, s16, 0x10000
	s_addc_u32 s17, s17, 0
	s_waitcnt vmcnt(22)
	v_lshlrev_b32_e32 v16, 16, v234
	v_and_b32_e32 v17, 0xffff0000, v234
	v_lshlrev_b32_e32 v18, 16, v235
	v_and_b32_e32 v19, 0xffff0000, v235
	v_pk_fma_f32 v[10:11], v[10:11], v[238:239], v[16:17]
	v_pk_fma_f32 v[12:13], v[12:13], v[240:241], v[18:19]
	global_load_dwordx2 v[234:235], v4, s[14:15]
	global_load_dwordx4 v[238:241], v2, s[18:19]
	s_add_u32 s14, s14, 0x10000
	s_addc_u32 s15, s15, 0
	s_add_u32 s18, s18, 0x200
	s_addc_u32 s19, s19, 0
	v_cvt_pk_bf16_f32 v6, v10, v11
	v_cvt_pk_bf16_f32 v7, v12, v13
	global_store_dwordx2 v4, v[6:7], s[16:17]
	s_add_u32 s16, s16, 0x10000
	s_addc_u32 s17, s17, 0
	s_waitcnt vmcnt(22)
	v_lshlrev_b32_e32 v16, 16, v242
	v_and_b32_e32 v17, 0xffff0000, v242
	v_lshlrev_b32_e32 v18, 16, v243
	v_and_b32_e32 v19, 0xffff0000, v243
	v_pk_fma_f32 v[10:11], v[10:11], v[198:199], v[16:17]
	v_pk_fma_f32 v[12:13], v[12:13], v[200:201], v[18:19]
	global_load_dwordx2 v[242:243], v4, s[14:15]
	global_load_dwordx4 v[198:201], v2, s[18:19]
	s_add_u32 s14, s14, 0x10000
	s_addc_u32 s15, s15, 0
	s_add_u32 s18, s18, 0x200
	s_addc_u32 s19, s19, 0
	v_cvt_pk_bf16_f32 v8, v10, v11
	v_cvt_pk_bf16_f32 v9, v12, v13
	global_store_dwordx2 v4, v[8:9], s[16:17]
	s_add_u32 s16, s16, 0x10000
	s_addc_u32 s17, s17, 0
	s_waitcnt vmcnt(22)
	v_lshlrev_b32_e32 v16, 16, v244
	v_and_b32_e32 v17, 0xffff0000, v244
	v_lshlrev_b32_e32 v18, 16, v245
	v_and_b32_e32 v19, 0xffff0000, v245
	v_pk_fma_f32 v[10:11], v[10:11], v[202:203], v[16:17]
	v_pk_fma_f32 v[12:13], v[12:13], v[204:205], v[18:19]
	global_load_dwordx2 v[244:245], v4, s[14:15]
	global_load_dwordx4 v[202:205], v2, s[18:19]
	s_add_u32 s14, s14, 0x10000
	s_addc_u32 s15, s15, 0
	s_add_u32 s18, s18, 0x200
	s_addc_u32 s19, s19, 0
	v_cvt_pk_bf16_f32 v6, v10, v11
	v_cvt_pk_bf16_f32 v7, v12, v13
	global_store_dwordx2 v4, v[6:7], s[16:17]
	s_add_u32 s16, s16, 0x10000
	s_addc_u32 s17, s17, 0
	s_waitcnt vmcnt(22)
	v_lshlrev_b32_e32 v16, 16, v246
	v_and_b32_e32 v17, 0xffff0000, v246
	v_lshlrev_b32_e32 v18, 16, v247
	v_and_b32_e32 v19, 0xffff0000, v247
	v_pk_fma_f32 v[10:11], v[10:11], v[206:207], v[16:17]
	v_pk_fma_f32 v[12:13], v[12:13], v[208:209], v[18:19]
	global_load_dwordx2 v[246:247], v4, s[14:15]
	global_load_dwordx4 v[206:209], v2, s[18:19]
	s_add_u32 s14, s14, 0x10000
	s_addc_u32 s15, s15, 0
	s_add_u32 s18, s18, 0x200
	s_addc_u32 s19, s19, 0
	v_cvt_pk_bf16_f32 v8, v10, v11
	v_cvt_pk_bf16_f32 v9, v12, v13
	global_store_dwordx2 v4, v[8:9], s[16:17]
	s_add_u32 s16, s16, 0x10000
	s_addc_u32 s17, s17, 0
	s_waitcnt vmcnt(22)
	v_lshlrev_b32_e32 v16, 16, v248
	v_and_b32_e32 v17, 0xffff0000, v248
	v_lshlrev_b32_e32 v18, 16, v249
	v_and_b32_e32 v19, 0xffff0000, v249
	v_pk_fma_f32 v[10:11], v[10:11], v[218:219], v[16:17]
	v_pk_fma_f32 v[12:13], v[12:13], v[220:221], v[18:19]
	global_load_dwordx2 v[248:249], v4, s[14:15]
	global_load_dwordx4 v[218:221], v2, s[18:19]
	s_add_u32 s14, s14, 0x10000
	s_addc_u32 s15, s15, 0
	s_add_u32 s18, s18, 0x200
	s_addc_u32 s19, s19, 0
	v_cvt_pk_bf16_f32 v6, v10, v11
	v_cvt_pk_bf16_f32 v7, v12, v13
	global_store_dwordx2 v4, v[6:7], s[16:17]
	s_add_u32 s16, s16, 0x10000
	s_addc_u32 s17, s17, 0
	s_waitcnt vmcnt(22)
	v_lshlrev_b32_e32 v16, 16, v250
	v_and_b32_e32 v17, 0xffff0000, v250
	v_lshlrev_b32_e32 v18, 16, v251
	v_and_b32_e32 v19, 0xffff0000, v251
	v_pk_fma_f32 v[10:11], v[10:11], v[222:223], v[16:17]
	v_pk_fma_f32 v[12:13], v[12:13], v[224:225], v[18:19]
	global_load_dwordx2 v[250:251], v4, s[14:15]
	global_load_dwordx4 v[222:225], v2, s[18:19]
	s_add_u32 s14, s14, 0x10000
	s_addc_u32 s15, s15, 0
	s_add_u32 s18, s18, 0x200
	s_addc_u32 s19, s19, 0
	v_cvt_pk_bf16_f32 v8, v10, v11
	v_cvt_pk_bf16_f32 v9, v12, v13
	global_store_dwordx2 v4, v[8:9], s[16:17]
	s_add_u32 s16, s16, 0x10000
	s_addc_u32 s17, s17, 0
	s_waitcnt vmcnt(22)
	v_lshlrev_b32_e32 v16, 16, v252
	v_and_b32_e32 v17, 0xffff0000, v252
	v_lshlrev_b32_e32 v18, 16, v253
	v_and_b32_e32 v19, 0xffff0000, v253
	v_pk_fma_f32 v[10:11], v[10:11], v[226:227], v[16:17]
	v_pk_fma_f32 v[12:13], v[12:13], v[228:229], v[18:19]
	global_load_dwordx2 v[252:253], v4, s[14:15]
	global_load_dwordx4 v[226:229], v2, s[18:19]
	s_add_u32 s14, s14, 0x10000
	s_addc_u32 s15, s15, 0
	s_add_u32 s18, s18, 0x200
	s_addc_u32 s19, s19, 0
	v_cvt_pk_bf16_f32 v6, v10, v11
	v_cvt_pk_bf16_f32 v7, v12, v13
	global_store_dwordx2 v4, v[6:7], s[16:17]
	s_add_u32 s16, s16, 0x10000
	s_addc_u32 s17, s17, 0
	s_waitcnt vmcnt(22)
	v_lshlrev_b32_e32 v16, 16, v212
	v_and_b32_e32 v17, 0xffff0000, v212
	v_lshlrev_b32_e32 v18, 16, v213
	v_and_b32_e32 v19, 0xffff0000, v213
	v_pk_fma_f32 v[10:11], v[10:11], v[230:231], v[16:17]
	v_pk_fma_f32 v[12:13], v[12:13], v[232:233], v[18:19]
	global_load_dwordx2 v[212:213], v4, s[14:15]
	global_load_dwordx4 v[230:233], v2, s[18:19]
	s_add_u32 s14, s14, 0x10000
	s_addc_u32 s15, s15, 0
	s_add_u32 s18, s18, 0x200
	s_addc_u32 s19, s19, 0
	v_cvt_pk_bf16_f32 v8, v10, v11
	v_cvt_pk_bf16_f32 v9, v12, v13
	global_store_dwordx2 v4, v[8:9], s[16:17]
	s_add_u32 s16, s16, 0x10000
	s_addc_u32 s17, s17, 0
	s_waitcnt vmcnt(22)
	v_lshlrev_b32_e32 v16, 16, v234
	v_and_b32_e32 v17, 0xffff0000, v234
	v_lshlrev_b32_e32 v18, 16, v235
	v_and_b32_e32 v19, 0xffff0000, v235
	v_pk_fma_f32 v[10:11], v[10:11], v[238:239], v[16:17]
	v_pk_fma_f32 v[12:13], v[12:13], v[240:241], v[18:19]
	v_cvt_pk_bf16_f32 v6, v10, v11
	v_cvt_pk_bf16_f32 v7, v12, v13
	global_store_dwordx2 v4, v[6:7], s[16:17]
	s_add_u32 s16, s16, 0x10000
	s_addc_u32 s17, s17, 0
	s_waitcnt vmcnt(20)
	v_lshlrev_b32_e32 v16, 16, v242
	v_and_b32_e32 v17, 0xffff0000, v242
	v_lshlrev_b32_e32 v18, 16, v243
	v_and_b32_e32 v19, 0xffff0000, v243
	v_pk_fma_f32 v[10:11], v[10:11], v[198:199], v[16:17]
	v_pk_fma_f32 v[12:13], v[12:13], v[200:201], v[18:19]
	v_cvt_pk_bf16_f32 v8, v10, v11
	v_cvt_pk_bf16_f32 v9, v12, v13
	global_store_dwordx2 v4, v[8:9], s[16:17]
	s_add_u32 s16, s16, 0x10000
	s_addc_u32 s17, s17, 0
	s_waitcnt vmcnt(18)
	v_lshlrev_b32_e32 v16, 16, v244
	v_and_b32_e32 v17, 0xffff0000, v244
	v_lshlrev_b32_e32 v18, 16, v245
	v_and_b32_e32 v19, 0xffff0000, v245
	v_pk_fma_f32 v[10:11], v[10:11], v[202:203], v[16:17]
	v_pk_fma_f32 v[12:13], v[12:13], v[204:205], v[18:19]
	v_cvt_pk_bf16_f32 v6, v10, v11
	v_cvt_pk_bf16_f32 v7, v12, v13
	global_store_dwordx2 v4, v[6:7], s[16:17]
	s_add_u32 s16, s16, 0x10000
	s_addc_u32 s17, s17, 0
	s_waitcnt vmcnt(16)
	v_lshlrev_b32_e32 v16, 16, v246
	v_and_b32_e32 v17, 0xffff0000, v246
	v_lshlrev_b32_e32 v18, 16, v247
	v_and_b32_e32 v19, 0xffff0000, v247
	v_pk_fma_f32 v[10:11], v[10:11], v[206:207], v[16:17]
	v_pk_fma_f32 v[12:13], v[12:13], v[208:209], v[18:19]
	v_cvt_pk_bf16_f32 v8, v10, v11
	v_cvt_pk_bf16_f32 v9, v12, v13
	global_store_dwordx2 v4, v[8:9], s[16:17]
	s_add_u32 s16, s16, 0x10000
	s_addc_u32 s17, s17, 0
	s_waitcnt vmcnt(14)
	v_lshlrev_b32_e32 v16, 16, v248
	v_and_b32_e32 v17, 0xffff0000, v248
	v_lshlrev_b32_e32 v18, 16, v249
	v_and_b32_e32 v19, 0xffff0000, v249
	v_pk_fma_f32 v[10:11], v[10:11], v[218:219], v[16:17]
	v_pk_fma_f32 v[12:13], v[12:13], v[220:221], v[18:19]
	v_cvt_pk_bf16_f32 v6, v10, v11
	v_cvt_pk_bf16_f32 v7, v12, v13
	global_store_dwordx2 v4, v[6:7], s[16:17]
	s_add_u32 s16, s16, 0x10000
	s_addc_u32 s17, s17, 0
	s_waitcnt vmcnt(12)
	v_lshlrev_b32_e32 v16, 16, v250
	v_and_b32_e32 v17, 0xffff0000, v250
	v_lshlrev_b32_e32 v18, 16, v251
	v_and_b32_e32 v19, 0xffff0000, v251
	v_pk_fma_f32 v[10:11], v[10:11], v[222:223], v[16:17]
	v_pk_fma_f32 v[12:13], v[12:13], v[224:225], v[18:19]
	v_cvt_pk_bf16_f32 v8, v10, v11
	v_cvt_pk_bf16_f32 v9, v12, v13
	global_store_dwordx2 v4, v[8:9], s[16:17]
	s_add_u32 s16, s16, 0x10000
	s_addc_u32 s17, s17, 0
	s_waitcnt vmcnt(10)
	v_lshlrev_b32_e32 v16, 16, v252
	v_and_b32_e32 v17, 0xffff0000, v252
	v_lshlrev_b32_e32 v18, 16, v253
	v_and_b32_e32 v19, 0xffff0000, v253
	v_pk_fma_f32 v[10:11], v[10:11], v[226:227], v[16:17]
	v_pk_fma_f32 v[12:13], v[12:13], v[228:229], v[18:19]
	v_cvt_pk_bf16_f32 v6, v10, v11
	v_cvt_pk_bf16_f32 v7, v12, v13
	global_store_dwordx2 v4, v[6:7], s[16:17]
	s_add_u32 s16, s16, 0x10000
	s_addc_u32 s17, s17, 0
	s_waitcnt vmcnt(8)
	v_lshlrev_b32_e32 v16, 16, v212
	v_and_b32_e32 v17, 0xffff0000, v212
	v_lshlrev_b32_e32 v18, 16, v213
	v_and_b32_e32 v19, 0xffff0000, v213
	v_pk_fma_f32 v[10:11], v[10:11], v[230:231], v[16:17]
	v_pk_fma_f32 v[12:13], v[12:13], v[232:233], v[18:19]
	v_cvt_pk_bf16_f32 v8, v10, v11
	v_cvt_pk_bf16_f32 v9, v12, v13
	global_store_dwordx2 v4, v[8:9], s[16:17]
	v_add_u32_e32 v1, s10, v1
	v_cmp_lt_i32_e32 vcc, s31, v1
	s_or_b64 s[4:5], vcc, s[4:5]
	v_add_u32_e32 v14, s11, v14
	s_andn2_b64 exec, exec, s[4:5]
	s_cbranch_execnz .LBB0_358

.LBB0_837:
	s_or_b64 exec, exec, s[8:9]
	v_add_u32_e32 v10, 0x800, v93
	ds_write2_b32 v10, v6, v2 offset1:16
	ds_write2_b32 v10, v7, v3 offset0:32 offset1:48
	ds_write2_b32 v10, v8, v4 offset0:64 offset1:80
	ds_write2_b32 v10, v9, v5 offset0:96 offset1:112
	v_add_u32_e32 v6, 0x8000, v36
	s_waitcnt lgkmcnt(0)
	s_barrier
	ds_read2_b32 v[2:3], v6 offset1:32
	v_add_u32_e32 v4, v35, v37
	ds_read_b32 v4, v4
	ds_read_b32 v7, v74
	ds_read_b32 v10, v75
	ds_read_b32 v11, v76
	ds_read_b32 v12, v77
	ds_read_b32 v13, v78
	ds_read_b32 v14, v79
	ds_read_b32 v15, v80
	s_waitcnt lgkmcnt(7)
	v_add_f32_e32 v8, 0, v4
	ds_read2_b32 v[4:5], v6 offset0:64 offset1:96
	v_add_f32_e32 v2, 0, v2
	v_add_f32_e32 v16, v2, v3
	ds_read2_b32 v[2:3], v6 offset0:128 offset1:160
	s_waitcnt lgkmcnt(8)
	v_add_f32_e32 v7, v8, v7
	ds_read2_b32 v[8:9], v6 offset0:192 offset1:224
	s_waitcnt lgkmcnt(2)
	v_add_f32_e32 v4, v16, v4
	v_add_f32_e32 v4, v4, v5
	s_waitcnt lgkmcnt(1)
	v_add_f32_e32 v2, v4, v2
	v_add_f32_e32 v2, v2, v3
	s_waitcnt lgkmcnt(0)
	v_add_f32_e32 v2, v2, v8
	v_add_f32_e32 v2, v2, v9
	v_fmamk_f32 v2, v2, 0x3a000000, v81
	v_mul_f32_e32 v3, 0x4f800000, v2
	v_cmp_gt_f32_e32 vcc, s26, v2
	v_add_f32_e32 v4, v7, v10
	v_add_f32_e32 v4, v4, v11
	v_cndmask_b32_e32 v2, v2, v3, vcc
	v_sqrt_f32_e32 v3, v2
	v_add_f32_e32 v4, v4, v12
	v_add_f32_e32 v4, v4, v13
	v_add_f32_e32 v4, v4, v14
	v_add_u32_e32 v5, -1, v3
	v_fma_f32 v7, -v5, v3, v2
	v_cmp_ge_f32_e64 s[8:9], 0, v7
	v_add_u32_e32 v7, 1, v3
	v_add_f32_e32 v4, v4, v15
	v_cndmask_b32_e64 v5, v3, v5, s[8:9]
	v_fma_f32 v3, -v7, v3, v2
	v_cmp_lt_f32_e64 s[8:9], 0, v3
	v_mov_b32_e32 v10, 1
	s_nop 0
	v_cndmask_b32_e64 v3, v5, v7, s[8:9]
	v_mul_f32_e32 v5, 0x37800000, v3
	v_cndmask_b32_e32 v3, v3, v5, vcc
	v_cmp_class_f32_e32 vcc, v2, v82
	s_nop 1
	v_cndmask_b32_e32 v2, v3, v2, vcc
	v_div_scale_f32 v3, s[8:9], v2, v2, 1.0
	v_rcp_f32_e32 v5, v3
	s_nop 0
	v_fma_f32 v7, -v3, v5, 1.0
	v_fmac_f32_e32 v5, v7, v5
	v_div_scale_f32 v7, vcc, 1.0, v2, 1.0
	v_mul_f32_e32 v8, v7, v5
	v_fma_f32 v9, -v3, v8, v7
	v_fmac_f32_e32 v8, v9, v5
	v_fma_f32 v3, -v3, v8, v7
	v_div_fmas_f32 v3, v3, v5, v8
	v_div_fixup_f32 v7, v3, v2, 1.0
	v_fma_f32 v2, v4, v7, v56
	v_cmp_o_f32_e32 vcc, v2, v2
	v_mov_b32_e32 v9, 1
	s_nop 0
	v_cndmask_b32_e32 v8, v94, v2, vcc
	ds_write_b32 v71, v8 offset:36864
	s_waitcnt lgkmcnt(0)
	ds_read_b128 v[2:5], v20 offset:36864
	s_waitcnt lgkmcnt(0)
	v_cmp_eq_f32_e32 vcc, v2, v8
	s_nop 1
	v_cndmask_b32_e32 v10, 0, v38, vcc
	v_cmp_gt_f32_e32 vcc, v2, v8
	s_nop 1
	v_cndmask_b32_e64 v10, v10, 1, vcc
	v_cmp_eq_f32_e32 vcc, v3, v8
	s_nop 1
	v_cndmask_b32_e32 v9, 0, v39, vcc
	v_cmp_gt_f32_e32 vcc, v3, v8
	s_nop 1
	v_cndmask_b32_e64 v9, v9, 1, vcc
	v_mov_b32_e32 v11, 1
	v_mov_b32_e32 v12, 1
	v_cmp_eq_f32_e32 vcc, v4, v8
	s_nop 1
	v_cndmask_b32_e32 v12, 0, v40, vcc
	v_cmp_gt_f32_e32 vcc, v4, v8
	s_nop 1
	v_cndmask_b32_e64 v12, v12, 1, vcc
	v_cmp_eq_f32_e32 vcc, v5, v8
	s_nop 1
	v_cndmask_b32_e32 v11, 0, v41, vcc
	v_cmp_gt_f32_e32 vcc, v5, v8
	s_nop 1
	v_cndmask_b32_e64 v11, v11, 1, vcc
	ds_read_b128 v[2:5], v20 offset:36880
	v_mov_b32_e32 v13, 1
	v_mov_b32_e32 v14, 1
	s_waitcnt lgkmcnt(0)
	v_cmp_eq_f32_e32 vcc, v2, v8
	s_nop 1
	v_cndmask_b32_e32 v14, 0, v42, vcc
	v_cmp_gt_f32_e32 vcc, v2, v8
	s_nop 1
	v_cndmask_b32_e64 v14, v14, 1, vcc
	v_cmp_eq_f32_e32 vcc, v3, v8
	s_nop 1
	v_cndmask_b32_e32 v13, 0, v43, vcc
	v_cmp_gt_f32_e32 vcc, v3, v8
	s_nop 1
	v_cndmask_b32_e64 v13, v13, 1, vcc
	v_mov_b32_e32 v15, 1
	v_mov_b32_e32 v16, 1
	v_cmp_eq_f32_e32 vcc, v4, v8
	s_nop 1
	v_cndmask_b32_e32 v16, 0, v44, vcc
	v_cmp_gt_f32_e32 vcc, v4, v8
	s_nop 1
	v_cndmask_b32_e64 v16, v16, 1, vcc
	v_cmp_eq_f32_e32 vcc, v5, v8
	s_nop 1
	v_cndmask_b32_e32 v15, 0, v45, vcc
	v_cmp_gt_f32_e32 vcc, v5, v8
	s_nop 1
	v_cndmask_b32_e64 v15, v15, 1, vcc
	ds_read_b128 v[2:5], v20 offset:36896
	v_mov_b32_e32 v17, 1
	v_mov_b32_e32 v25, 1
	s_waitcnt lgkmcnt(0)
	v_cmp_eq_f32_e32 vcc, v2, v8
	s_nop 1
	v_cndmask_b32_e32 v25, 0, v46, vcc
	v_cmp_gt_f32_e32 vcc, v2, v8
	s_nop 1
	v_cndmask_b32_e64 v25, v25, 1, vcc
	v_cmp_eq_f32_e32 vcc, v3, v8
	s_nop 1
	v_cndmask_b32_e32 v17, 0, v47, vcc
	v_cmp_gt_f32_e32 vcc, v3, v8
	s_nop 1
	v_cndmask_b32_e64 v17, v17, 1, vcc
	v_mov_b32_e32 v26, 1
	v_mov_b32_e32 v27, 1
	v_cmp_eq_f32_e32 vcc, v4, v8
	s_nop 1
	v_cndmask_b32_e32 v27, 0, v48, vcc
	v_cmp_gt_f32_e32 vcc, v4, v8
	s_nop 1
	v_cndmask_b32_e64 v27, v27, 1, vcc
	v_cmp_eq_f32_e32 vcc, v5, v8
	s_nop 1
	v_cndmask_b32_e32 v26, 0, v49, vcc
	v_cmp_gt_f32_e32 vcc, v5, v8
	s_nop 1
	v_cndmask_b32_e64 v26, v26, 1, vcc
	ds_read_b128 v[2:5], v20 offset:36912
	v_mov_b32_e32 v28, 1
	v_mov_b32_e32 v29, 1
	s_waitcnt lgkmcnt(0)
	v_cmp_eq_f32_e32 vcc, v2, v8
	s_nop 1
	v_cndmask_b32_e32 v29, 0, v50, vcc
	v_cmp_gt_f32_e32 vcc, v2, v8
	s_nop 1
	v_cndmask_b32_e64 v29, v29, 1, vcc
	v_cmp_eq_f32_e32 vcc, v3, v8
	s_nop 1
	v_cndmask_b32_e32 v28, 0, v51, vcc
	v_cmp_gt_f32_e32 vcc, v3, v8
	s_nop 1
	v_cndmask_b32_e64 v28, v28, 1, vcc
	v_mov_b32_e32 v30, 1
	v_mov_b32_e32 v31, 1
	v_cmp_eq_f32_e32 vcc, v4, v8
	s_nop 1
	v_cndmask_b32_e32 v31, 0, v52, vcc
	v_cmp_gt_f32_e32 vcc, v4, v8
	s_nop 1
	v_cndmask_b32_e64 v31, v31, 1, vcc
	v_cmp_eq_f32_e32 vcc, v5, v8
	s_nop 1
	v_cndmask_b32_e32 v30, 0, v53, vcc
	v_cmp_gt_f32_e32 vcc, v5, v8
	s_nop 1
	v_cndmask_b32_e64 v30, v30, 1, vcc
	ds_read_b128 v[2:5], v20 offset:36928
	v_mov_b32_e32 v32, 1
	v_mov_b32_e32 v33, 1
	s_waitcnt lgkmcnt(0)
	v_cmp_eq_f32_e32 vcc, v2, v8
	s_nop 1
	v_cndmask_b32_e32 v33, 0, v54, vcc
	v_cmp_gt_f32_e32 vcc, v2, v8
	s_nop 1
	v_cndmask_b32_e64 v33, v33, 1, vcc
	v_cmp_eq_f32_e32 vcc, v3, v8
	s_nop 1
	v_cndmask_b32_e32 v32, 0, v55, vcc
	v_cmp_gt_f32_e32 vcc, v3, v8
	s_nop 1
	v_cndmask_b32_e64 v32, v32, 1, vcc
	v_mov_b32_e32 v95, 1
	v_mov_b32_e32 v96, 1
	v_cmp_eq_f32_e32 vcc, v4, v8
	s_nop 1
	v_cndmask_b32_e32 v96, 0, v57, vcc
	v_cmp_gt_f32_e32 vcc, v4, v8
	s_nop 1
	v_cndmask_b32_e64 v96, v96, 1, vcc
	v_cmp_eq_f32_e32 vcc, v5, v8
	s_nop 1
	v_cndmask_b32_e32 v95, 0, v58, vcc
	v_cmp_gt_f32_e32 vcc, v5, v8
	s_nop 1
	v_cndmask_b32_e64 v95, v95, 1, vcc
	ds_read_b128 v[2:5], v20 offset:36944
	v_mov_b32_e32 v97, 1
	v_mov_b32_e32 v98, 1
	s_waitcnt lgkmcnt(0)
	v_cmp_eq_f32_e32 vcc, v2, v8
	s_nop 1
	v_cndmask_b32_e32 v98, 0, v59, vcc
	v_cmp_gt_f32_e32 vcc, v2, v8
	s_nop 1
	v_cndmask_b32_e64 v98, v98, 1, vcc
	v_cmp_eq_f32_e32 vcc, v3, v8
	s_nop 1
	v_cndmask_b32_e32 v97, 0, v60, vcc
	v_cmp_gt_f32_e32 vcc, v3, v8
	s_nop 1
	v_cndmask_b32_e64 v97, v97, 1, vcc
	v_mov_b32_e32 v99, 1
	v_mov_b32_e32 v100, 1
	v_cmp_eq_f32_e32 vcc, v4, v8
	s_nop 1
	v_cndmask_b32_e32 v100, 0, v61, vcc
	v_cmp_gt_f32_e32 vcc, v4, v8
	s_nop 1
	v_cndmask_b32_e64 v100, v100, 1, vcc
	v_cmp_eq_f32_e32 vcc, v5, v8
	s_nop 1
	v_cndmask_b32_e32 v99, 0, v62, vcc
	v_cmp_gt_f32_e32 vcc, v5, v8
	s_nop 1
	v_cndmask_b32_e64 v99, v99, 1, vcc
	ds_read_b128 v[2:5], v20 offset:36960
	v_mov_b32_e32 v101, 1
	v_mov_b32_e32 v102, 1
	s_waitcnt lgkmcnt(0)
	v_cmp_eq_f32_e32 vcc, v2, v8
	s_nop 1
	v_cndmask_b32_e32 v102, 0, v63, vcc
	v_cmp_gt_f32_e32 vcc, v2, v8
	s_nop 1
	v_cndmask_b32_e64 v102, v102, 1, vcc
	v_cmp_eq_f32_e32 vcc, v3, v8
	s_nop 1
	v_cndmask_b32_e32 v101, 0, v64, vcc
	v_cmp_gt_f32_e32 vcc, v3, v8
	s_nop 1
	v_cndmask_b32_e64 v101, v101, 1, vcc
	v_mov_b32_e32 v103, 1
	v_mov_b32_e32 v104, 1
	v_cmp_eq_f32_e32 vcc, v4, v8
	s_nop 1
	v_cndmask_b32_e32 v104, 0, v65, vcc
	v_cmp_gt_f32_e32 vcc, v4, v8
	s_nop 1
	v_cndmask_b32_e64 v104, v104, 1, vcc
	v_cmp_eq_f32_e32 vcc, v5, v8
	s_nop 1
	v_cndmask_b32_e32 v103, 0, v66, vcc
	v_cmp_gt_f32_e32 vcc, v5, v8
	s_nop 1
	v_cndmask_b32_e64 v103, v103, 1, vcc
	ds_read_b128 v[2:5], v20 offset:36976
	v_mov_b32_e32 v105, 1
	v_mov_b32_e32 v106, 1
	s_waitcnt lgkmcnt(0)
	v_cmp_eq_f32_e32 vcc, v2, v8
	s_nop 1
	v_cndmask_b32_e32 v106, 0, v67, vcc
	v_cmp_gt_f32_e32 vcc, v2, v8
	s_nop 1
	v_cndmask_b32_e64 v106, v106, 1, vcc
	v_cmp_eq_f32_e32 vcc, v3, v8
	s_nop 1
	v_cndmask_b32_e32 v105, 0, v68, vcc
	v_cmp_gt_f32_e32 vcc, v3, v8
	s_nop 1
	v_cndmask_b32_e64 v105, v105, 1, vcc
	v_mov_b32_e32 v2, 1
	v_cmp_eq_f32_e32 vcc, v4, v8
	s_nop 1
	v_cndmask_b32_e32 v2, 0, v69, vcc
	v_cmp_gt_f32_e32 vcc, v4, v8
	s_nop 1
	v_cndmask_b32_e64 v2, v2, 1, vcc
	v_add3_u32 v3, v9, v10, v12
	v_add3_u32 v3, v3, v11, v14
	v_add3_u32 v3, v3, v13, v16
	v_add3_u32 v3, v3, v15, v25
	v_add3_u32 v3, v3, v17, v27
	v_add3_u32 v3, v3, v26, v29
	v_add3_u32 v3, v3, v28, v31
	v_add3_u32 v3, v3, v30, v33
	v_add3_u32 v3, v3, v32, v96
	v_add3_u32 v3, v3, v95, v98
	v_add3_u32 v3, v3, v97, v100
	v_add3_u32 v3, v3, v99, v102
	v_add3_u32 v3, v3, v101, v104
	v_cmp_gt_f32_e32 vcc, v5, v8
	s_nop 1
	v_addc_co_u32_e32 v3, vcc, v3, v103, vcc
	v_add_u32_e32 v3, v3, v106
	v_add3_u32 v3, v3, v105, v2
	v_cmp_gt_u32_e32 vcc, 4, v3
	s_and_saveexec_b64 s[8:9], vcc
	v_lshl_add_u32 v2, v3, 2, v22
	ds_write_b32 v2, v8 offset:40960
	s_or_b64 exec, exec, s[8:9]
	s_waitcnt lgkmcnt(0)
	v_add_u32_e32 v2, s28, v34
	s_and_saveexec_b64 s[8:9], vcc
	s_cbranch_execz .LBB0_965
	ds_read_b128 v[10:13], v22 offset:40960
	s_waitcnt lgkmcnt(0)
	v_sub_f32_e32 v9, v11, v10
	v_sub_f32_e32 v5, v12, v10
	v_mul_f32_e32 v9, 0x3fb8aa3b, v9
	v_sub_f32_e32 v4, v13, v10
	v_mul_f32_e32 v5, 0x3fb8aa3b, v5
	v_exp_f32_e32 v9, v9
	v_mul_f32_e32 v4, 0x3fb8aa3b, v4
	v_exp_f32_e32 v5, v5
	v_exp_f32_e32 v4, v4
	v_add_f32_e32 v9, 1.0, v9
	v_add_f32_e32 v5, v5, v9
	v_add_f32_e32 v4, v4, v5
	v_div_scale_f32 v5, s[24:25], v4, v4, 1.0
	v_rcp_f32_e32 v9, v5
	v_div_scale_f32 v11, vcc, 1.0, v4, 1.0
	v_fma_f32 v12, -v5, v9, 1.0
	v_fmac_f32_e32 v9, v12, v9
	v_mul_f32_e32 v12, v11, v9
	v_fma_f32 v13, -v5, v12, v11
	v_fmac_f32_e32 v12, v13, v9
	v_fma_f32 v5, -v5, v12, v11
	v_div_fmas_f32 v5, v5, v9, v12
	v_div_fixup_f32 v11, v5, v4, 1.0
	v_lshl_or_b32 v4, v2, 2, v3
	v_sub_f32_e32 v3, v8, v10
	v_mul_f32_e32 v3, 0x3fb8aa3b, v3
	v_exp_f32_e32 v3, v3
	v_ashrrev_i32_e32 v5, 31, v4
	v_lshlrev_b64 v[4:5], 2, v[4:5]
	v_lshl_add_u64 v[8:9], s[16:17], 0, v[4:5]
	v_mul_f32_e32 v3, v3, v11
	v_lshl_add_u64 v[4:5], s[18:19], 0, v[4:5]
	global_store_dword v[8:9], v21, off
	global_store_dword v[4:5], v3, off
	ds_add_u32 v35, v83 offset:33792

.LBB0_967:
	s_or_b64 exec, exec, s[8:9]
	s_waitcnt lgkmcnt(0)
	ds_read2_b32 v[2:3], v6 offset0:2 offset1:34
	ds_read_b32 v4, v84
	ds_read_b32 v7, v85
	ds_read_b32 v8, v86
	ds_read_b32 v9, v87
	ds_read_b32 v10, v88
	ds_read_b32 v11, v89
	ds_read_b32 v12, v90
	ds_read_b32 v13, v91
	s_waitcnt lgkmcnt(7)
	v_add_f32_e32 v14, 0, v4
	ds_read2_b32 v[4:5], v6 offset0:66 offset1:98
	s_waitcnt lgkmcnt(7)
	v_add_f32_e32 v14, v14, v7
	v_add_f32_e32 v2, 0, v2
	v_add_f32_e32 v15, v2, v3
	ds_read2_b32 v[2:3], v6 offset0:130 offset1:162
	ds_read2_b32 v[6:7], v6 offset0:194 offset1:226
	s_waitcnt lgkmcnt(2)
	v_add_f32_e32 v4, v15, v4
	v_add_f32_e32 v4, v4, v5
	s_waitcnt lgkmcnt(1)
	v_add_f32_e32 v2, v4, v2
	v_add_f32_e32 v2, v2, v3
	s_waitcnt lgkmcnt(0)
	v_add_f32_e32 v2, v2, v6
	v_add_f32_e32 v2, v2, v7
	v_fmamk_f32 v2, v2, 0x3a000000, v81
	v_mul_f32_e32 v3, 0x4f800000, v2
	v_cmp_gt_f32_e32 vcc, s26, v2
	v_add_f32_e32 v4, v14, v8
	v_add_f32_e32 v4, v4, v9
	v_cndmask_b32_e32 v2, v2, v3, vcc
	v_sqrt_f32_e32 v3, v2
	v_add_f32_e32 v4, v4, v10
	v_add_f32_e32 v4, v4, v11
	v_add_f32_e32 v4, v4, v12
	v_add_u32_e32 v5, -1, v3
	v_fma_f32 v6, -v5, v3, v2
	v_cmp_ge_f32_e64 s[8:9], 0, v6
	v_add_u32_e32 v6, 1, v3
	v_add_f32_e32 v4, v4, v13
	v_cndmask_b32_e64 v5, v3, v5, s[8:9]
	v_fma_f32 v3, -v6, v3, v2
	v_cmp_lt_f32_e64 s[8:9], 0, v3
	v_mov_b32_e32 v9, 1
	s_nop 0
	v_cndmask_b32_e64 v3, v5, v6, s[8:9]
	v_mul_f32_e32 v5, 0x37800000, v3
	v_cndmask_b32_e32 v3, v3, v5, vcc
	v_cmp_class_f32_e32 vcc, v2, v82
	s_nop 1
	v_cndmask_b32_e32 v2, v3, v2, vcc
	v_div_scale_f32 v3, s[8:9], v2, v2, 1.0
	v_rcp_f32_e32 v5, v3
	s_nop 0
	v_fma_f32 v6, -v3, v5, 1.0
	v_fmac_f32_e32 v5, v6, v5
	v_div_scale_f32 v6, vcc, 1.0, v2, 1.0
	v_mul_f32_e32 v7, v6, v5
	v_fma_f32 v8, -v3, v7, v6
	v_fmac_f32_e32 v7, v8, v5
	v_fma_f32 v3, -v3, v7, v6
	v_div_fmas_f32 v3, v3, v5, v7
	v_div_fixup_f32 v6, v3, v2, 1.0
	v_fma_f32 v2, v4, v6, v56
	v_cmp_o_f32_e32 vcc, v2, v2
	v_mov_b32_e32 v8, 1
	s_nop 0
	v_cndmask_b32_e32 v7, v94, v2, vcc
	ds_write_b32 v71, v7 offset:36864
	s_waitcnt lgkmcnt(0)
	ds_read_b128 v[2:5], v20 offset:36864
	s_waitcnt lgkmcnt(0)
	v_cmp_eq_f32_e32 vcc, v2, v7
	s_nop 1
	v_cndmask_b32_e32 v9, 0, v38, vcc
	v_cmp_gt_f32_e32 vcc, v2, v7
	s_nop 1
	v_cndmask_b32_e64 v9, v9, 1, vcc
	v_cmp_eq_f32_e32 vcc, v3, v7
	s_nop 1
	v_cndmask_b32_e32 v8, 0, v39, vcc
	v_cmp_gt_f32_e32 vcc, v3, v7
	s_nop 1
	v_cndmask_b32_e64 v8, v8, 1, vcc
	v_mov_b32_e32 v10, 1
	v_mov_b32_e32 v11, 1
	v_cmp_eq_f32_e32 vcc, v4, v7
	s_nop 1
	v_cndmask_b32_e32 v11, 0, v40, vcc
	v_cmp_gt_f32_e32 vcc, v4, v7
	s_nop 1
	v_cndmask_b32_e64 v11, v11, 1, vcc
	v_cmp_eq_f32_e32 vcc, v5, v7
	s_nop 1
	v_cndmask_b32_e32 v10, 0, v41, vcc
	v_cmp_gt_f32_e32 vcc, v5, v7
	s_nop 1
	v_cndmask_b32_e64 v10, v10, 1, vcc
	ds_read_b128 v[2:5], v20 offset:36880
	v_mov_b32_e32 v12, 1
	v_mov_b32_e32 v13, 1
	s_waitcnt lgkmcnt(0)
	v_cmp_eq_f32_e32 vcc, v2, v7
	s_nop 1
	v_cndmask_b32_e32 v13, 0, v42, vcc
	v_cmp_gt_f32_e32 vcc, v2, v7
	s_nop 1
	v_cndmask_b32_e64 v13, v13, 1, vcc
	v_cmp_eq_f32_e32 vcc, v3, v7
	s_nop 1
	v_cndmask_b32_e32 v12, 0, v43, vcc
	v_cmp_gt_f32_e32 vcc, v3, v7
	s_nop 1
	v_cndmask_b32_e64 v12, v12, 1, vcc
	v_mov_b32_e32 v14, 1
	v_mov_b32_e32 v15, 1
	v_cmp_eq_f32_e32 vcc, v4, v7
	s_nop 1
	v_cndmask_b32_e32 v15, 0, v44, vcc
	v_cmp_gt_f32_e32 vcc, v4, v7
	s_nop 1
	v_cndmask_b32_e64 v15, v15, 1, vcc
	v_cmp_eq_f32_e32 vcc, v5, v7
	s_nop 1
	v_cndmask_b32_e32 v14, 0, v45, vcc
	v_cmp_gt_f32_e32 vcc, v5, v7
	s_nop 1
	v_cndmask_b32_e64 v14, v14, 1, vcc
	ds_read_b128 v[2:5], v20 offset:36896
	v_mov_b32_e32 v16, 1
	v_mov_b32_e32 v17, 1
	s_waitcnt lgkmcnt(0)
	v_cmp_eq_f32_e32 vcc, v2, v7
	s_nop 1
	v_cndmask_b32_e32 v17, 0, v46, vcc
	v_cmp_gt_f32_e32 vcc, v2, v7
	s_nop 1
	v_cndmask_b32_e64 v17, v17, 1, vcc
	v_cmp_eq_f32_e32 vcc, v3, v7
	s_nop 1
	v_cndmask_b32_e32 v16, 0, v47, vcc
	v_cmp_gt_f32_e32 vcc, v3, v7
	s_nop 1
	v_cndmask_b32_e64 v16, v16, 1, vcc
	v_mov_b32_e32 v25, 1
	v_mov_b32_e32 v26, 1
	v_cmp_eq_f32_e32 vcc, v4, v7
	s_nop 1
	v_cndmask_b32_e32 v26, 0, v48, vcc
	v_cmp_gt_f32_e32 vcc, v4, v7
	s_nop 1
	v_cndmask_b32_e64 v26, v26, 1, vcc
	v_cmp_eq_f32_e32 vcc, v5, v7
	s_nop 1
	v_cndmask_b32_e32 v25, 0, v49, vcc
	v_cmp_gt_f32_e32 vcc, v5, v7
	s_nop 1
	v_cndmask_b32_e64 v25, v25, 1, vcc
	ds_read_b128 v[2:5], v20 offset:36912
	v_mov_b32_e32 v27, 1
	v_mov_b32_e32 v28, 1
	s_waitcnt lgkmcnt(0)
	v_cmp_eq_f32_e32 vcc, v2, v7
	s_nop 1
	v_cndmask_b32_e32 v28, 0, v50, vcc
	v_cmp_gt_f32_e32 vcc, v2, v7
	s_nop 1
	v_cndmask_b32_e64 v28, v28, 1, vcc
	v_cmp_eq_f32_e32 vcc, v3, v7
	s_nop 1
	v_cndmask_b32_e32 v27, 0, v51, vcc
	v_cmp_gt_f32_e32 vcc, v3, v7
	s_nop 1
	v_cndmask_b32_e64 v27, v27, 1, vcc
	v_mov_b32_e32 v29, 1
	v_mov_b32_e32 v30, 1
	v_cmp_eq_f32_e32 vcc, v4, v7
	s_nop 1
	v_cndmask_b32_e32 v30, 0, v52, vcc
	v_cmp_gt_f32_e32 vcc, v4, v7
	s_nop 1
	v_cndmask_b32_e64 v30, v30, 1, vcc
	v_cmp_eq_f32_e32 vcc, v5, v7
	s_nop 1
	v_cndmask_b32_e32 v29, 0, v53, vcc
	v_cmp_gt_f32_e32 vcc, v5, v7
	s_nop 1
	v_cndmask_b32_e64 v29, v29, 1, vcc
	ds_read_b128 v[2:5], v20 offset:36928
	v_mov_b32_e32 v31, 1
	v_mov_b32_e32 v32, 1
	s_waitcnt lgkmcnt(0)
	v_cmp_eq_f32_e32 vcc, v2, v7
	s_nop 1
	v_cndmask_b32_e32 v32, 0, v54, vcc
	v_cmp_gt_f32_e32 vcc, v2, v7
	s_nop 1
	v_cndmask_b32_e64 v32, v32, 1, vcc
	v_cmp_eq_f32_e32 vcc, v3, v7
	s_nop 1
	v_cndmask_b32_e32 v31, 0, v55, vcc
	v_cmp_gt_f32_e32 vcc, v3, v7
	s_nop 1
	v_cndmask_b32_e64 v31, v31, 1, vcc
	v_mov_b32_e32 v33, 1
	v_mov_b32_e32 v95, 1
	v_cmp_eq_f32_e32 vcc, v4, v7
	s_nop 1
	v_cndmask_b32_e32 v95, 0, v57, vcc
	v_cmp_gt_f32_e32 vcc, v4, v7
	s_nop 1
	v_cndmask_b32_e64 v95, v95, 1, vcc
	v_cmp_eq_f32_e32 vcc, v5, v7
	s_nop 1
	v_cndmask_b32_e32 v33, 0, v58, vcc
	v_cmp_gt_f32_e32 vcc, v5, v7
	s_nop 1
	v_cndmask_b32_e64 v33, v33, 1, vcc
	ds_read_b128 v[2:5], v20 offset:36944
	v_mov_b32_e32 v96, 1
	v_mov_b32_e32 v97, 1
	s_waitcnt lgkmcnt(0)
	v_cmp_eq_f32_e32 vcc, v2, v7
	s_nop 1
	v_cndmask_b32_e32 v97, 0, v59, vcc
	v_cmp_gt_f32_e32 vcc, v2, v7
	s_nop 1
	v_cndmask_b32_e64 v97, v97, 1, vcc
	v_cmp_eq_f32_e32 vcc, v3, v7
	s_nop 1
	v_cndmask_b32_e32 v96, 0, v60, vcc
	v_cmp_gt_f32_e32 vcc, v3, v7
	s_nop 1
	v_cndmask_b32_e64 v96, v96, 1, vcc
	v_mov_b32_e32 v98, 1
	v_mov_b32_e32 v99, 1
	v_cmp_eq_f32_e32 vcc, v4, v7
	s_nop 1
	v_cndmask_b32_e32 v99, 0, v61, vcc
	v_cmp_gt_f32_e32 vcc, v4, v7
	s_nop 1
	v_cndmask_b32_e64 v99, v99, 1, vcc
	v_cmp_eq_f32_e32 vcc, v5, v7
	s_nop 1
	v_cndmask_b32_e32 v98, 0, v62, vcc
	v_cmp_gt_f32_e32 vcc, v5, v7
	s_nop 1
	v_cndmask_b32_e64 v98, v98, 1, vcc
	ds_read_b128 v[2:5], v20 offset:36960
	v_mov_b32_e32 v100, 1
	v_mov_b32_e32 v101, 1
	s_waitcnt lgkmcnt(0)
	v_cmp_eq_f32_e32 vcc, v2, v7
	s_nop 1
	v_cndmask_b32_e32 v101, 0, v63, vcc
	v_cmp_gt_f32_e32 vcc, v2, v7
	s_nop 1
	v_cndmask_b32_e64 v101, v101, 1, vcc
	v_cmp_eq_f32_e32 vcc, v3, v7
	s_nop 1
	v_cndmask_b32_e32 v100, 0, v64, vcc
	v_cmp_gt_f32_e32 vcc, v3, v7
	s_nop 1
	v_cndmask_b32_e64 v100, v100, 1, vcc
	v_mov_b32_e32 v102, 1
	v_mov_b32_e32 v103, 1
	v_cmp_eq_f32_e32 vcc, v4, v7
	s_nop 1
	v_cndmask_b32_e32 v103, 0, v65, vcc
	v_cmp_gt_f32_e32 vcc, v4, v7
	s_nop 1
	v_cndmask_b32_e64 v103, v103, 1, vcc
	v_cmp_eq_f32_e32 vcc, v5, v7
	s_nop 1
	v_cndmask_b32_e32 v102, 0, v66, vcc
	v_cmp_gt_f32_e32 vcc, v5, v7
	s_nop 1
	v_cndmask_b32_e64 v102, v102, 1, vcc
	ds_read_b128 v[2:5], v20 offset:36976
	v_mov_b32_e32 v104, 1
	v_mov_b32_e32 v105, 1
	s_waitcnt lgkmcnt(0)
	v_cmp_eq_f32_e32 vcc, v2, v7
	s_nop 1
	v_cndmask_b32_e32 v105, 0, v67, vcc
	v_cmp_gt_f32_e32 vcc, v2, v7
	s_nop 1
	v_cndmask_b32_e64 v105, v105, 1, vcc
	v_cmp_eq_f32_e32 vcc, v3, v7
	s_nop 1
	v_cndmask_b32_e32 v104, 0, v68, vcc
	v_cmp_gt_f32_e32 vcc, v3, v7
	s_nop 1
	v_cndmask_b32_e64 v104, v104, 1, vcc
	v_mov_b32_e32 v2, 1
	v_cmp_eq_f32_e32 vcc, v4, v7
	s_nop 1
	v_cndmask_b32_e32 v2, 0, v69, vcc
	v_cmp_gt_f32_e32 vcc, v4, v7
	s_nop 1
	v_cndmask_b32_e64 v2, v2, 1, vcc
	v_add3_u32 v3, v8, v9, v11
	v_add3_u32 v3, v3, v10, v13
	v_add3_u32 v3, v3, v12, v15
	v_add3_u32 v3, v3, v14, v17
	v_add3_u32 v3, v3, v16, v26
	v_add3_u32 v3, v3, v25, v28
	v_add3_u32 v3, v3, v27, v30
	v_add3_u32 v3, v3, v29, v32
	v_add3_u32 v3, v3, v31, v95
	v_add3_u32 v3, v3, v33, v97
	v_add3_u32 v3, v3, v96, v99
	v_add3_u32 v3, v3, v98, v101
	v_add3_u32 v3, v3, v100, v103
	v_cmp_gt_f32_e32 vcc, v5, v7
	s_nop 1
	v_addc_co_u32_e32 v3, vcc, v3, v102, vcc
	v_add_u32_e32 v3, v3, v105
	v_add3_u32 v3, v3, v104, v2
	v_cmp_gt_u32_e32 vcc, 4, v3
	s_and_saveexec_b64 s[8:9], vcc
	v_lshl_add_u32 v2, v3, 2, v22
	ds_write_b32 v2, v7 offset:40960
	s_or_b64 exec, exec, s[8:9]
	s_waitcnt lgkmcnt(0)
	v_add_u32_e32 v2, s28, v70
	s_and_saveexec_b64 s[8:9], vcc
	s_cbranch_execz .LBB0_1095
	ds_read_b128 v[8:11], v22 offset:40960
	s_waitcnt lgkmcnt(0)
	v_sub_f32_e32 v9, v9, v8
	v_sub_f32_e32 v5, v10, v8
	v_mul_f32_e32 v9, 0x3fb8aa3b, v9
	v_sub_f32_e32 v4, v11, v8
	v_mul_f32_e32 v5, 0x3fb8aa3b, v5
	v_exp_f32_e32 v9, v9
	v_mul_f32_e32 v4, 0x3fb8aa3b, v4
	v_exp_f32_e32 v5, v5
	v_exp_f32_e32 v4, v4
	v_add_f32_e32 v9, 1.0, v9
	v_add_f32_e32 v5, v5, v9
	v_add_f32_e32 v4, v4, v5
	v_div_scale_f32 v5, s[24:25], v4, v4, 1.0
	v_rcp_f32_e32 v9, v5
	v_div_scale_f32 v10, vcc, 1.0, v4, 1.0
	v_fma_f32 v11, -v5, v9, 1.0
	v_fmac_f32_e32 v9, v11, v9
	v_mul_f32_e32 v11, v10, v9
	v_fma_f32 v12, -v5, v11, v10
	v_fmac_f32_e32 v11, v12, v9
	v_fma_f32 v5, -v5, v11, v10
	v_div_fmas_f32 v5, v5, v9, v11
	v_div_fixup_f32 v10, v5, v4, 1.0
	v_lshl_or_b32 v4, v2, 2, v3
	v_sub_f32_e32 v3, v7, v8
	v_mul_f32_e32 v3, 0x3fb8aa3b, v3
	v_exp_f32_e32 v3, v3
	v_ashrrev_i32_e32 v5, 31, v4
	v_lshlrev_b64 v[4:5], 2, v[4:5]
	v_lshl_add_u64 v[8:9], s[16:17], 0, v[4:5]
	v_mul_f32_e32 v3, v3, v10
	v_lshl_add_u64 v[4:5], s[18:19], 0, v[4:5]
	global_store_dword v[8:9], v21, off
	global_store_dword v[4:5], v3, off
	ds_add_u32 v35, v83 offset:33792
